# v063
# speedup vs baseline: 1.1467x; 1.0056x over previous
.LBB2_45:
	s_and_b64 vcc, exec, s[28:29]
	s_cbranch_vccnz .Lmy_epi_last
	s_cmp_eq_u32 s30, 7
	s_cbranch_scc1 .Lmy_epi_nl7
	v_exp_f32_e32 v124, v124
	v_exp_f32_e32 v125, v125
	v_exp_f32_e32 v126, v126
	v_pk_add_f32 v[124:125], v[124:125], 1.0 op_sel_hi:[1,0]
	v_exp_f32_e32 v127, v127
	v_exp_f32_e32 v120, v120
	v_pk_add_f32 v[126:127], v[126:127], 1.0 op_sel_hi:[1,0]
	v_exp_f32_e32 v121, v121
	v_exp_f32_e32 v122, v122
	v_pk_fma_f32 v[120:121], v[120:121], v[124:125], v[124:125]
	v_exp_f32_e32 v123, v123
	v_exp_f32_e32 v116, v116
	v_pk_fma_f32 v[122:123], v[122:123], v[126:127], v[126:127]
	v_exp_f32_e32 v117, v117
	v_pk_add_f32 v[124:125], v[124:125], 2.0 op_sel_hi:[1,0] neg_lo:[1,0] neg_hi:[1,0]
	v_exp_f32_e32 v118, v118
	v_pk_add_f32 v[126:127], v[126:127], 2.0 op_sel_hi:[1,0] neg_lo:[1,0] neg_hi:[1,0]
	v_exp_f32_e32 v119, v119
	v_pk_fma_f32 v[124:125], v[124:125], v[116:117], v[124:125]
	v_pk_fma_f32 v[116:117], v[116:117], v[120:121], v[120:121]
	v_pk_fma_f32 v[126:127], v[126:127], v[118:119], v[126:127]
	v_pk_fma_f32 v[118:119], v[118:119], v[122:123], v[122:123]
	v_rcp_f32_e32 v116, v116
	v_rcp_f32_e32 v117, v117
	v_rcp_f32_e32 v118, v118
	v_rcp_f32_e32 v119, v119
	s_waitcnt lgkmcnt(3)
	v_pk_fma_f32 v[124:125], v[172:173], v[120:121], v[124:125]
	v_pk_fma_f32 v[126:127], v[174:175], v[122:123], v[126:127]
	v_pk_mul_f32 v[116:117], v[116:117], v[124:125]
	v_pk_mul_f32 v[118:119], v[118:119], v[126:127]
	global_store_dwordx4 v[176:177], v[116:119], off nt
	s_nop 1
	v_pk_mul_f32 v[116:117], v[116:117], s[96:97] op_sel_hi:[1,0]
	v_pk_mul_f32 v[118:119], v[118:119], s[96:97] op_sel_hi:[1,0]
	v_exp_f32_e32 v112, v112
	v_exp_f32_e32 v113, v113
	v_exp_f32_e32 v114, v114
	v_pk_fma_f32 v[112:113], v[112:113], s[98:99], s[98:99] op_sel_hi:[1,0,0]
	v_exp_f32_e32 v115, v115
	v_exp_f32_e32 v116, v116
	v_pk_fma_f32 v[114:115], v[114:115], s[98:99], s[98:99] op_sel_hi:[1,0,0]
	v_exp_f32_e32 v117, v117
	v_exp_f32_e32 v118, v118
	v_pk_fma_f32 v[112:113], v[116:117], v[112:113], v[112:113]
	v_exp_f32_e32 v119, v119
	v_pk_add_f32 v[116:117], v[116:117], 1.0 op_sel_hi:[1,0] neg_lo:[1,0] neg_hi:[1,0]
	v_rcp_f32_e32 v112, v112
	v_rcp_f32_e32 v113, v113
	v_pk_fma_f32 v[114:115], v[118:119], v[114:115], v[114:115]
	v_pk_add_f32 v[118:119], v[118:119], 1.0 op_sel_hi:[1,0] neg_lo:[1,0] neg_hi:[1,0]
	v_rcp_f32_e32 v114, v114
	v_rcp_f32_e32 v115, v115
	v_pk_mul_f32 v[112:113], v[112:113], v[116:117]
	v_pk_mul_f32 v[114:115], v[114:115], v[118:119]
	v_cvt_pk_fp8_f32 v124, v112, v113
	s_add_u32 s0, s8, s27
	s_addc_u32 s1, s9, 0
	s_ashr_i32 s35, s34, 31
	s_lshl_b64 s[34:35], s[34:35], 21
	v_ashrrev_i32_e32 v209, 31, v208
	s_add_u32 s36, s73, s34
	v_lshrrev_b32_e32 v126, 4, v210
	v_and_b32_e32 v127, 15, v210
	v_lshl_or_b32 v126, v126, 8, v127
	v_and_b32_e32 v127, 15, v208
	v_mul_u32_u24_e32 v127, 0x3f0, v127
	v_sub_u32_e32 v126, v126, v127
	v_ashrrev_i32_e32 v127, 31, v126
	v_lshl_add_u64 v[122:123], s[0:1], 0, v[126:127]
	v_cvt_pk_fp8_f32 v124, v114, v115 op_sel:[0,0,1]
	v_lshlrev_b64 v[116:117], 10, v[208:209]
	s_addc_u32 s37, s74, s35
	v_lshl_add_u64 v[118:119], v[122:123], 0, v[116:117]
	global_store_dword v[118:119], v124, off
	s_cmp_eq_u32 s30, 7
	s_cselect_b64 s[34:35], -1, 0
	s_cmp_lg_u32 s30, 7
	v_lshrrev_b32_e32 v126, 4, v210
	v_lshlrev_b32_e32 v126, 9, v126
	v_and_b32_e32 v127, 15, v210
	v_lshl_or_b32 v126, v127, 1, v126
	v_and_b32_e32 v127, 15, v208
	v_mul_u32_u24_e32 v127, 0x7e0, v127
	v_sub_u32_e32 v126, v126, v127
	v_ashrrev_i32_e32 v127, 31, v126
	v_lshl_add_u64 v[120:121], s[36:37], 0, v[126:127]
	v_exp_f32_e32 v108, v108
	v_exp_f32_e32 v109, v109
	v_exp_f32_e32 v110, v110
	v_pk_add_f32 v[108:109], v[108:109], 1.0 op_sel_hi:[1,0]
	v_exp_f32_e32 v111, v111
	v_exp_f32_e32 v104, v104
	v_pk_add_f32 v[110:111], v[110:111], 1.0 op_sel_hi:[1,0]
	v_exp_f32_e32 v105, v105
	v_exp_f32_e32 v106, v106
	v_pk_fma_f32 v[104:105], v[104:105], v[108:109], v[108:109]
	v_exp_f32_e32 v107, v107
	v_exp_f32_e32 v100, v100
	v_pk_fma_f32 v[106:107], v[106:107], v[110:111], v[110:111]
	v_exp_f32_e32 v101, v101
	v_pk_add_f32 v[108:109], v[108:109], 2.0 op_sel_hi:[1,0] neg_lo:[1,0] neg_hi:[1,0]
	v_exp_f32_e32 v102, v102
	v_pk_add_f32 v[110:111], v[110:111], 2.0 op_sel_hi:[1,0] neg_lo:[1,0] neg_hi:[1,0]
	v_exp_f32_e32 v103, v103
	v_pk_fma_f32 v[108:109], v[108:109], v[100:101], v[108:109]
	v_pk_fma_f32 v[100:101], v[100:101], v[104:105], v[104:105]
	v_pk_fma_f32 v[110:111], v[110:111], v[102:103], v[110:111]
	v_pk_fma_f32 v[102:103], v[102:103], v[106:107], v[106:107]
	v_rcp_f32_e32 v100, v100
	v_rcp_f32_e32 v101, v101
	v_rcp_f32_e32 v102, v102
	v_rcp_f32_e32 v103, v103
	s_waitcnt lgkmcnt(2)
	v_pk_fma_f32 v[108:109], v[168:169], v[104:105], v[108:109]
	v_pk_fma_f32 v[110:111], v[170:171], v[106:107], v[110:111]
	v_lshl_add_u64 v[104:105], v[176:177], 0, s[18:19]
	v_pk_mul_f32 v[100:101], v[100:101], v[108:109]
	v_pk_mul_f32 v[102:103], v[102:103], v[110:111]
	global_store_dwordx4 v[104:105], v[100:103], off nt
	s_nop 1
	v_pk_mul_f32 v[100:101], v[100:101], s[96:97] op_sel_hi:[1,0]
	v_pk_mul_f32 v[102:103], v[102:103], s[96:97] op_sel_hi:[1,0]
	v_exp_f32_e32 v96, v96
	v_exp_f32_e32 v97, v97
	v_exp_f32_e32 v98, v98
	v_pk_fma_f32 v[96:97], v[96:97], s[98:99], s[98:99] op_sel_hi:[1,0,0]
	v_exp_f32_e32 v99, v99
	v_exp_f32_e32 v100, v100
	v_pk_fma_f32 v[98:99], v[98:99], s[98:99], s[98:99] op_sel_hi:[1,0,0]
	v_exp_f32_e32 v101, v101
	v_exp_f32_e32 v102, v102
	v_pk_fma_f32 v[96:97], v[100:101], v[96:97], v[96:97]
	v_exp_f32_e32 v103, v103
	v_pk_add_f32 v[100:101], v[100:101], 1.0 op_sel_hi:[1,0] neg_lo:[1,0] neg_hi:[1,0]
	v_rcp_f32_e32 v96, v96
	v_rcp_f32_e32 v97, v97
	v_pk_fma_f32 v[98:99], v[102:103], v[98:99], v[98:99]
	v_pk_add_f32 v[102:103], v[102:103], 1.0 op_sel_hi:[1,0] neg_lo:[1,0] neg_hi:[1,0]
	v_rcp_f32_e32 v98, v98
	v_rcp_f32_e32 v99, v99
	v_pk_mul_f32 v[96:97], v[96:97], v[100:101]
	v_pk_mul_f32 v[98:99], v[98:99], v[102:103]
	v_cvt_pk_fp8_f32 v104, v96, v97
	v_ashrrev_i32_e32 v207, 31, v206
	v_lshlrev_b64 v[100:101], 10, v[206:207]
	v_lshl_add_u64 v[102:103], v[122:123], 0, v[100:101]
	v_cvt_pk_fp8_f32 v104, v98, v99 op_sel:[0,0,1]
	v_cndmask_b32_e64 v105, 0, 1, s[34:35]
	global_store_dword v[102:103], v104, off
	v_cmp_ne_u32_e64 s[0:1], 1, v105
	v_exp_f32_e32 v92, v92
	v_exp_f32_e32 v93, v93
	v_exp_f32_e32 v94, v94
	v_pk_add_f32 v[92:93], v[92:93], 1.0 op_sel_hi:[1,0]
	v_exp_f32_e32 v95, v95
	v_exp_f32_e32 v88, v88
	v_pk_add_f32 v[94:95], v[94:95], 1.0 op_sel_hi:[1,0]
	v_exp_f32_e32 v89, v89
	v_exp_f32_e32 v90, v90
	v_pk_fma_f32 v[88:89], v[88:89], v[92:93], v[92:93]
	v_exp_f32_e32 v91, v91
	v_exp_f32_e32 v84, v84
	v_pk_fma_f32 v[90:91], v[90:91], v[94:95], v[94:95]
	v_exp_f32_e32 v85, v85
	v_pk_add_f32 v[92:93], v[92:93], 2.0 op_sel_hi:[1,0] neg_lo:[1,0] neg_hi:[1,0]
	v_exp_f32_e32 v86, v86
	v_pk_add_f32 v[94:95], v[94:95], 2.0 op_sel_hi:[1,0] neg_lo:[1,0] neg_hi:[1,0]
	v_exp_f32_e32 v87, v87
	v_pk_fma_f32 v[92:93], v[92:93], v[84:85], v[92:93]
	v_pk_fma_f32 v[84:85], v[84:85], v[88:89], v[88:89]
	v_pk_fma_f32 v[94:95], v[94:95], v[86:87], v[94:95]
	v_pk_fma_f32 v[86:87], v[86:87], v[90:91], v[90:91]
	v_rcp_f32_e32 v84, v84
	v_rcp_f32_e32 v85, v85
	v_rcp_f32_e32 v86, v86
	v_rcp_f32_e32 v87, v87
	s_waitcnt lgkmcnt(1)
	v_pk_fma_f32 v[92:93], v[164:165], v[88:89], v[92:93]
	v_pk_fma_f32 v[94:95], v[166:167], v[90:91], v[94:95]
	v_pk_mul_f32 v[84:85], v[84:85], v[92:93]
	v_pk_mul_f32 v[86:87], v[86:87], v[94:95]
	v_lshl_add_u64 v[88:89], v[176:177], 0, s[12:13]
	global_store_dwordx4 v[88:89], v[84:87], off nt
	s_nop 1
	v_pk_mul_f32 v[84:85], v[84:85], s[96:97] op_sel_hi:[1,0]
	v_pk_mul_f32 v[86:87], v[86:87], s[96:97] op_sel_hi:[1,0]
	v_exp_f32_e32 v80, v80
	v_exp_f32_e32 v81, v81
	v_exp_f32_e32 v82, v82
	v_pk_fma_f32 v[80:81], v[80:81], s[98:99], s[98:99] op_sel_hi:[1,0,0]
	v_exp_f32_e32 v83, v83
	v_exp_f32_e32 v84, v84
	v_pk_fma_f32 v[82:83], v[82:83], s[98:99], s[98:99] op_sel_hi:[1,0,0]
	v_exp_f32_e32 v85, v85
	v_exp_f32_e32 v86, v86
	v_pk_fma_f32 v[80:81], v[84:85], v[80:81], v[80:81]
	v_exp_f32_e32 v87, v87
	v_pk_add_f32 v[84:85], v[84:85], 1.0 op_sel_hi:[1,0] neg_lo:[1,0] neg_hi:[1,0]
	v_rcp_f32_e32 v80, v80
	v_rcp_f32_e32 v81, v81
	v_pk_fma_f32 v[82:83], v[86:87], v[82:83], v[82:83]
	v_pk_add_f32 v[86:87], v[86:87], 1.0 op_sel_hi:[1,0] neg_lo:[1,0] neg_hi:[1,0]
	v_rcp_f32_e32 v82, v82
	v_rcp_f32_e32 v83, v83
	v_pk_mul_f32 v[80:81], v[80:81], v[84:85]
	v_pk_mul_f32 v[82:83], v[82:83], v[86:87]
	v_ashrrev_i32_e32 v205, 31, v204
	v_cvt_pk_fp8_f32 v88, v80, v81
	s_and_b64 vcc, exec, s[0:1]
	v_cvt_pk_fp8_f32 v88, v82, v83 op_sel:[0,0,1]
	v_lshlrev_b64 v[84:85], 10, v[204:205]
	v_lshl_add_u64 v[86:87], v[122:123], 0, v[84:85]
	global_store_dword v[86:87], v88, off
	v_exp_f32_e32 v76, v76
	v_exp_f32_e32 v77, v77
	v_exp_f32_e32 v78, v78
	v_pk_add_f32 v[76:77], v[76:77], 1.0 op_sel_hi:[1,0]
	v_exp_f32_e32 v79, v79
	v_exp_f32_e32 v72, v72
	v_pk_add_f32 v[78:79], v[78:79], 1.0 op_sel_hi:[1,0]
	v_exp_f32_e32 v73, v73
	v_exp_f32_e32 v74, v74
	v_pk_fma_f32 v[72:73], v[72:73], v[76:77], v[76:77]
	v_exp_f32_e32 v75, v75
	v_exp_f32_e32 v68, v68
	v_pk_fma_f32 v[74:75], v[74:75], v[78:79], v[78:79]
	v_exp_f32_e32 v69, v69
	v_pk_add_f32 v[76:77], v[76:77], 2.0 op_sel_hi:[1,0] neg_lo:[1,0] neg_hi:[1,0]
	v_exp_f32_e32 v70, v70
	v_pk_add_f32 v[78:79], v[78:79], 2.0 op_sel_hi:[1,0] neg_lo:[1,0] neg_hi:[1,0]
	v_exp_f32_e32 v71, v71
	v_pk_fma_f32 v[76:77], v[76:77], v[68:69], v[76:77]
	v_pk_fma_f32 v[68:69], v[68:69], v[72:73], v[72:73]
	v_pk_fma_f32 v[78:79], v[78:79], v[70:71], v[78:79]
	v_pk_fma_f32 v[70:71], v[70:71], v[74:75], v[74:75]
	v_rcp_f32_e32 v68, v68
	v_rcp_f32_e32 v69, v69
	v_rcp_f32_e32 v70, v70
	v_rcp_f32_e32 v71, v71
	s_waitcnt lgkmcnt(0)
	v_pk_fma_f32 v[76:77], v[160:161], v[72:73], v[76:77]
	v_pk_fma_f32 v[78:79], v[162:163], v[74:75], v[78:79]
	v_lshl_add_u64 v[72:73], v[176:177], 0, s[20:21]
	v_pk_mul_f32 v[68:69], v[68:69], v[76:77]
	v_pk_mul_f32 v[70:71], v[70:71], v[78:79]
	global_store_dwordx4 v[72:73], v[68:71], off nt
	s_nop 1
	v_pk_mul_f32 v[68:69], v[68:69], s[96:97] op_sel_hi:[1,0]
	v_pk_mul_f32 v[70:71], v[70:71], s[96:97] op_sel_hi:[1,0]
	v_exp_f32_e32 v64, v64
	v_exp_f32_e32 v65, v65
	v_exp_f32_e32 v66, v66
	v_pk_fma_f32 v[64:65], v[64:65], s[98:99], s[98:99] op_sel_hi:[1,0,0]
	v_exp_f32_e32 v67, v67
	v_exp_f32_e32 v68, v68
	v_pk_fma_f32 v[66:67], v[66:67], s[98:99], s[98:99] op_sel_hi:[1,0,0]
	v_exp_f32_e32 v69, v69
	v_exp_f32_e32 v70, v70
	v_pk_fma_f32 v[64:65], v[68:69], v[64:65], v[64:65]
	v_exp_f32_e32 v71, v71
	v_pk_add_f32 v[68:69], v[68:69], 1.0 op_sel_hi:[1,0] neg_lo:[1,0] neg_hi:[1,0]
	v_rcp_f32_e32 v64, v64
	v_rcp_f32_e32 v65, v65
	v_pk_fma_f32 v[66:67], v[70:71], v[66:67], v[66:67]
	v_pk_add_f32 v[70:71], v[70:71], 1.0 op_sel_hi:[1,0] neg_lo:[1,0] neg_hi:[1,0]
	v_rcp_f32_e32 v66, v66
	v_rcp_f32_e32 v67, v67
	v_pk_mul_f32 v[64:65], v[64:65], v[68:69]
	v_pk_mul_f32 v[66:67], v[66:67], v[70:71]
	v_ashrrev_i32_e32 v203, 31, v202
	v_cvt_pk_fp8_f32 v72, v64, v65
	s_and_b64 vcc, exec, s[0:1]
	v_cvt_pk_fp8_f32 v72, v66, v67 op_sel:[0,0,1]
	v_lshlrev_b64 v[68:69], 10, v[202:203]
	v_lshl_add_u64 v[70:71], v[122:123], 0, v[68:69]
	global_store_dword v[70:71], v72, off
	v_exp_f32_e32 v60, v60
	v_exp_f32_e32 v61, v61
	v_exp_f32_e32 v62, v62
	v_pk_add_f32 v[60:61], v[60:61], 1.0 op_sel_hi:[1,0]
	v_exp_f32_e32 v63, v63
	v_exp_f32_e32 v56, v56
	v_pk_add_f32 v[62:63], v[62:63], 1.0 op_sel_hi:[1,0]
	v_exp_f32_e32 v57, v57
	v_exp_f32_e32 v58, v58
	v_pk_fma_f32 v[56:57], v[56:57], v[60:61], v[60:61]
	v_exp_f32_e32 v59, v59
	v_exp_f32_e32 v52, v52
	v_pk_fma_f32 v[58:59], v[58:59], v[62:63], v[62:63]
	v_exp_f32_e32 v53, v53
	v_pk_add_f32 v[60:61], v[60:61], 2.0 op_sel_hi:[1,0] neg_lo:[1,0] neg_hi:[1,0]
	v_exp_f32_e32 v54, v54
	v_pk_add_f32 v[62:63], v[62:63], 2.0 op_sel_hi:[1,0] neg_lo:[1,0] neg_hi:[1,0]
	v_exp_f32_e32 v55, v55
	v_pk_fma_f32 v[60:61], v[60:61], v[52:53], v[60:61]
	v_pk_fma_f32 v[52:53], v[52:53], v[56:57], v[56:57]
	v_pk_fma_f32 v[62:63], v[62:63], v[54:55], v[62:63]
	v_pk_fma_f32 v[54:55], v[54:55], v[58:59], v[58:59]
	v_rcp_f32_e32 v52, v52
	v_rcp_f32_e32 v53, v53
	v_rcp_f32_e32 v54, v54
	v_rcp_f32_e32 v55, v55
	s_waitcnt vmcnt(8)
	v_pk_fma_f32 v[60:61], v[156:157], v[56:57], v[60:61]
	v_pk_fma_f32 v[62:63], v[158:159], v[58:59], v[62:63]
	v_pk_mul_f32 v[52:53], v[52:53], v[60:61]
	v_pk_mul_f32 v[54:55], v[54:55], v[62:63]
	v_lshl_add_u64 v[56:57], v[176:177], 0, s[14:15]
	global_store_dwordx4 v[56:57], v[52:55], off nt
	s_nop 1
	v_pk_mul_f32 v[52:53], v[52:53], s[96:97] op_sel_hi:[1,0]
	v_pk_mul_f32 v[54:55], v[54:55], s[96:97] op_sel_hi:[1,0]
	v_exp_f32_e32 v48, v48
	v_exp_f32_e32 v49, v49
	v_exp_f32_e32 v50, v50
	v_pk_fma_f32 v[48:49], v[48:49], s[98:99], s[98:99] op_sel_hi:[1,0,0]
	v_exp_f32_e32 v51, v51
	v_exp_f32_e32 v52, v52
	v_pk_fma_f32 v[50:51], v[50:51], s[98:99], s[98:99] op_sel_hi:[1,0,0]
	v_exp_f32_e32 v53, v53
	v_exp_f32_e32 v54, v54
	v_pk_fma_f32 v[48:49], v[52:53], v[48:49], v[48:49]
	v_exp_f32_e32 v55, v55
	v_pk_add_f32 v[52:53], v[52:53], 1.0 op_sel_hi:[1,0] neg_lo:[1,0] neg_hi:[1,0]
	v_rcp_f32_e32 v48, v48
	v_rcp_f32_e32 v49, v49
	v_pk_fma_f32 v[50:51], v[54:55], v[50:51], v[50:51]
	v_pk_add_f32 v[54:55], v[54:55], 1.0 op_sel_hi:[1,0] neg_lo:[1,0] neg_hi:[1,0]
	v_rcp_f32_e32 v50, v50
	v_rcp_f32_e32 v51, v51
	v_pk_mul_f32 v[48:49], v[48:49], v[52:53]
	v_pk_mul_f32 v[50:51], v[50:51], v[54:55]
	v_ashrrev_i32_e32 v201, 31, v200
	v_cvt_pk_fp8_f32 v56, v48, v49
	s_and_b64 vcc, exec, s[0:1]
	v_cvt_pk_fp8_f32 v56, v50, v51 op_sel:[0,0,1]
	v_lshlrev_b64 v[52:53], 10, v[200:201]
	v_lshl_add_u64 v[54:55], v[122:123], 0, v[52:53]
	global_store_dword v[54:55], v56, off
	v_exp_f32_e32 v44, v44
	v_exp_f32_e32 v45, v45
	v_exp_f32_e32 v46, v46
	v_pk_add_f32 v[44:45], v[44:45], 1.0 op_sel_hi:[1,0]
	v_exp_f32_e32 v47, v47
	v_exp_f32_e32 v40, v40
	v_pk_add_f32 v[46:47], v[46:47], 1.0 op_sel_hi:[1,0]
	v_exp_f32_e32 v41, v41
	v_exp_f32_e32 v42, v42
	v_pk_fma_f32 v[40:41], v[40:41], v[44:45], v[44:45]
	v_exp_f32_e32 v43, v43
	v_exp_f32_e32 v36, v36
	v_pk_fma_f32 v[42:43], v[42:43], v[46:47], v[46:47]
	v_exp_f32_e32 v37, v37
	v_pk_add_f32 v[44:45], v[44:45], 2.0 op_sel_hi:[1,0] neg_lo:[1,0] neg_hi:[1,0]
	v_exp_f32_e32 v38, v38
	v_pk_add_f32 v[46:47], v[46:47], 2.0 op_sel_hi:[1,0] neg_lo:[1,0] neg_hi:[1,0]
	v_exp_f32_e32 v39, v39
	v_pk_fma_f32 v[44:45], v[44:45], v[36:37], v[44:45]
	v_pk_fma_f32 v[36:37], v[36:37], v[40:41], v[40:41]
	v_pk_fma_f32 v[46:47], v[46:47], v[38:39], v[46:47]
	v_pk_fma_f32 v[38:39], v[38:39], v[42:43], v[42:43]
	v_rcp_f32_e32 v36, v36
	v_rcp_f32_e32 v37, v37
	v_rcp_f32_e32 v38, v38
	v_rcp_f32_e32 v39, v39
	v_pk_fma_f32 v[44:45], v[152:153], v[40:41], v[44:45]
	v_pk_fma_f32 v[46:47], v[154:155], v[42:43], v[46:47]
	v_lshl_add_u64 v[40:41], v[176:177], 0, s[22:23]
	v_pk_mul_f32 v[36:37], v[36:37], v[44:45]
	v_pk_mul_f32 v[38:39], v[38:39], v[46:47]
	global_store_dwordx4 v[40:41], v[36:39], off nt
	s_nop 1
	v_pk_mul_f32 v[36:37], v[36:37], s[96:97] op_sel_hi:[1,0]
	v_pk_mul_f32 v[38:39], v[38:39], s[96:97] op_sel_hi:[1,0]
	v_exp_f32_e32 v32, v32
	v_exp_f32_e32 v33, v33
	v_exp_f32_e32 v34, v34
	v_pk_fma_f32 v[32:33], v[32:33], s[98:99], s[98:99] op_sel_hi:[1,0,0]
	v_exp_f32_e32 v35, v35
	v_exp_f32_e32 v36, v36
	v_pk_fma_f32 v[34:35], v[34:35], s[98:99], s[98:99] op_sel_hi:[1,0,0]
	v_exp_f32_e32 v37, v37
	v_exp_f32_e32 v38, v38
	v_pk_fma_f32 v[32:33], v[36:37], v[32:33], v[32:33]
	v_exp_f32_e32 v39, v39
	v_pk_add_f32 v[36:37], v[36:37], 1.0 op_sel_hi:[1,0] neg_lo:[1,0] neg_hi:[1,0]
	v_rcp_f32_e32 v32, v32
	v_rcp_f32_e32 v33, v33
	v_pk_fma_f32 v[34:35], v[38:39], v[34:35], v[34:35]
	v_pk_add_f32 v[38:39], v[38:39], 1.0 op_sel_hi:[1,0] neg_lo:[1,0] neg_hi:[1,0]
	v_rcp_f32_e32 v34, v34
	v_rcp_f32_e32 v35, v35
	v_pk_mul_f32 v[32:33], v[32:33], v[36:37]
	v_pk_mul_f32 v[34:35], v[34:35], v[38:39]
	v_cvt_pk_fp8_f32 v40, v32, v33
	v_or_b32_e32 v36, 16, v200
	v_ashrrev_i32_e32 v37, 31, v36
	v_lshlrev_b64 v[36:37], 10, v[36:37]
	v_cvt_pk_fp8_f32 v40, v34, v35 op_sel:[0,0,1]
	v_lshl_add_u64 v[38:39], v[122:123], 0, v[36:37]
	global_store_dword v[38:39], v40, off
	v_exp_f32_e32 v28, v28
	v_exp_f32_e32 v29, v29
	v_exp_f32_e32 v30, v30
	v_pk_add_f32 v[28:29], v[28:29], 1.0 op_sel_hi:[1,0]
	v_exp_f32_e32 v31, v31
	v_exp_f32_e32 v24, v24
	v_pk_add_f32 v[30:31], v[30:31], 1.0 op_sel_hi:[1,0]
	v_exp_f32_e32 v25, v25
	v_exp_f32_e32 v26, v26
	v_pk_fma_f32 v[24:25], v[24:25], v[28:29], v[28:29]
	v_exp_f32_e32 v27, v27
	v_exp_f32_e32 v20, v20
	v_pk_fma_f32 v[26:27], v[26:27], v[30:31], v[30:31]
	v_exp_f32_e32 v21, v21
	v_pk_add_f32 v[28:29], v[28:29], 2.0 op_sel_hi:[1,0] neg_lo:[1,0] neg_hi:[1,0]
	v_exp_f32_e32 v22, v22
	v_pk_add_f32 v[30:31], v[30:31], 2.0 op_sel_hi:[1,0] neg_lo:[1,0] neg_hi:[1,0]
	v_exp_f32_e32 v23, v23
	v_pk_fma_f32 v[28:29], v[28:29], v[20:21], v[28:29]
	v_pk_fma_f32 v[20:21], v[20:21], v[24:25], v[24:25]
	v_pk_fma_f32 v[30:31], v[30:31], v[22:23], v[30:31]
	v_pk_fma_f32 v[22:23], v[22:23], v[26:27], v[26:27]
	v_rcp_f32_e32 v20, v20
	v_rcp_f32_e32 v21, v21
	v_rcp_f32_e32 v22, v22
	v_rcp_f32_e32 v23, v23
	v_pk_fma_f32 v[28:29], v[148:149], v[24:25], v[28:29]
	v_pk_fma_f32 v[30:31], v[150:151], v[26:27], v[30:31]
	v_pk_mul_f32 v[20:21], v[20:21], v[28:29]
	v_pk_mul_f32 v[22:23], v[22:23], v[30:31]
	v_lshl_add_u64 v[24:25], v[176:177], 0, s[16:17]
	global_store_dwordx4 v[24:25], v[20:23], off nt
	s_nop 1
	v_pk_mul_f32 v[20:21], v[20:21], s[96:97] op_sel_hi:[1,0]
	v_pk_mul_f32 v[22:23], v[22:23], s[96:97] op_sel_hi:[1,0]
	v_exp_f32_e32 v16, v16
	v_exp_f32_e32 v17, v17
	v_exp_f32_e32 v18, v18
	v_pk_fma_f32 v[16:17], v[16:17], s[98:99], s[98:99] op_sel_hi:[1,0,0]
	v_exp_f32_e32 v19, v19
	v_exp_f32_e32 v20, v20
	v_pk_fma_f32 v[18:19], v[18:19], s[98:99], s[98:99] op_sel_hi:[1,0,0]
	v_exp_f32_e32 v21, v21
	v_exp_f32_e32 v22, v22
	v_pk_fma_f32 v[16:17], v[20:21], v[16:17], v[16:17]
	v_exp_f32_e32 v23, v23
	v_pk_add_f32 v[20:21], v[20:21], 1.0 op_sel_hi:[1,0] neg_lo:[1,0] neg_hi:[1,0]
	v_rcp_f32_e32 v16, v16
	v_rcp_f32_e32 v17, v17
	v_pk_fma_f32 v[18:19], v[22:23], v[18:19], v[18:19]
	v_pk_add_f32 v[22:23], v[22:23], 1.0 op_sel_hi:[1,0] neg_lo:[1,0] neg_hi:[1,0]
	v_rcp_f32_e32 v18, v18
	v_rcp_f32_e32 v19, v19
	v_pk_mul_f32 v[16:17], v[16:17], v[20:21]
	v_pk_mul_f32 v[18:19], v[18:19], v[22:23]
	v_cvt_pk_fp8_f32 v24, v16, v17
	v_or_b32_e32 v20, 32, v200
	v_ashrrev_i32_e32 v21, 31, v20
	v_lshlrev_b64 v[20:21], 10, v[20:21]
	v_cvt_pk_fp8_f32 v24, v18, v19 op_sel:[0,0,1]
	v_lshl_add_u64 v[22:23], v[122:123], 0, v[20:21]
	global_store_dword v[22:23], v24, off
	v_exp_f32_e32 v12, v12
	v_exp_f32_e32 v13, v13
	v_exp_f32_e32 v14, v14
	v_pk_add_f32 v[12:13], v[12:13], 1.0 op_sel_hi:[1,0]
	v_exp_f32_e32 v15, v15
	v_exp_f32_e32 v8, v8
	v_pk_add_f32 v[14:15], v[14:15], 1.0 op_sel_hi:[1,0]
	v_exp_f32_e32 v9, v9
	v_exp_f32_e32 v10, v10
	v_pk_fma_f32 v[8:9], v[8:9], v[12:13], v[12:13]
	v_exp_f32_e32 v11, v11
	v_exp_f32_e32 v4, v4
	v_pk_fma_f32 v[10:11], v[10:11], v[14:15], v[14:15]
	v_exp_f32_e32 v5, v5
	v_pk_add_f32 v[12:13], v[12:13], 2.0 op_sel_hi:[1,0] neg_lo:[1,0] neg_hi:[1,0]
	v_exp_f32_e32 v6, v6
	v_pk_add_f32 v[14:15], v[14:15], 2.0 op_sel_hi:[1,0] neg_lo:[1,0] neg_hi:[1,0]
	v_exp_f32_e32 v7, v7
	v_pk_fma_f32 v[12:13], v[12:13], v[4:5], v[12:13]
	v_pk_fma_f32 v[4:5], v[4:5], v[8:9], v[8:9]
	v_pk_fma_f32 v[14:15], v[14:15], v[6:7], v[14:15]
	v_pk_fma_f32 v[6:7], v[6:7], v[10:11], v[10:11]
	v_rcp_f32_e32 v4, v4
	v_rcp_f32_e32 v5, v5
	v_rcp_f32_e32 v6, v6
	v_rcp_f32_e32 v7, v7
	v_pk_fma_f32 v[12:13], v[144:145], v[8:9], v[12:13]
	v_pk_fma_f32 v[14:15], v[146:147], v[10:11], v[14:15]
	v_lshl_add_u64 v[8:9], v[176:177], 0, s[24:25]
	v_pk_mul_f32 v[4:5], v[4:5], v[12:13]
	v_pk_mul_f32 v[6:7], v[6:7], v[14:15]
	global_store_dwordx4 v[8:9], v[4:7], off nt
	s_nop 1
	v_pk_mul_f32 v[4:5], v[4:5], s[96:97] op_sel_hi:[1,0]
	v_pk_mul_f32 v[6:7], v[6:7], s[96:97] op_sel_hi:[1,0]
	v_exp_f32_e32 v0, v0
	v_exp_f32_e32 v1, v1
	v_exp_f32_e32 v2, v2
	v_pk_fma_f32 v[0:1], v[0:1], s[98:99], s[98:99] op_sel_hi:[1,0,0]
	v_exp_f32_e32 v3, v3
	v_exp_f32_e32 v4, v4
	v_pk_fma_f32 v[2:3], v[2:3], s[98:99], s[98:99] op_sel_hi:[1,0,0]
	v_exp_f32_e32 v5, v5
	v_exp_f32_e32 v6, v6
	v_pk_fma_f32 v[0:1], v[4:5], v[0:1], v[0:1]
	v_exp_f32_e32 v7, v7
	v_pk_add_f32 v[4:5], v[4:5], 1.0 op_sel_hi:[1,0] neg_lo:[1,0] neg_hi:[1,0]
	v_rcp_f32_e32 v0, v0
	v_rcp_f32_e32 v1, v1
	v_pk_fma_f32 v[2:3], v[6:7], v[2:3], v[2:3]
	v_pk_add_f32 v[6:7], v[6:7], 1.0 op_sel_hi:[1,0] neg_lo:[1,0] neg_hi:[1,0]
	v_rcp_f32_e32 v2, v2
	v_rcp_f32_e32 v3, v3
	v_pk_mul_f32 v[0:1], v[0:1], v[4:5]
	v_pk_mul_f32 v[2:3], v[2:3], v[6:7]
	v_cvt_pk_fp8_f32 v8, v0, v1
	v_or_b32_e32 v4, 48, v200
	v_ashrrev_i32_e32 v5, 31, v4
	v_lshlrev_b64 v[4:5], 10, v[4:5]
	v_cvt_pk_fp8_f32 v8, v2, v3 op_sel:[0,0,1]
	v_lshl_add_u64 v[6:7], v[122:123], 0, v[4:5]
	global_store_dword v[6:7], v8, off
	s_branch .LBB2_24
.Lmy_epi_nl7:
	v_exp_f32_e32 v124, v124
	v_exp_f32_e32 v125, v125
	v_exp_f32_e32 v126, v126
	v_pk_add_f32 v[124:125], v[124:125], 1.0 op_sel_hi:[1,0]
	v_exp_f32_e32 v127, v127
	v_exp_f32_e32 v120, v120
	v_pk_add_f32 v[126:127], v[126:127], 1.0 op_sel_hi:[1,0]
	v_exp_f32_e32 v121, v121
	v_exp_f32_e32 v122, v122
	v_pk_fma_f32 v[120:121], v[120:121], v[124:125], v[124:125]
	v_exp_f32_e32 v123, v123
	v_exp_f32_e32 v116, v116
	v_pk_fma_f32 v[122:123], v[122:123], v[126:127], v[126:127]
	v_exp_f32_e32 v117, v117
	v_pk_add_f32 v[124:125], v[124:125], 2.0 op_sel_hi:[1,0] neg_lo:[1,0] neg_hi:[1,0]
	v_exp_f32_e32 v118, v118
	v_pk_add_f32 v[126:127], v[126:127], 2.0 op_sel_hi:[1,0] neg_lo:[1,0] neg_hi:[1,0]
	v_exp_f32_e32 v119, v119
	v_pk_fma_f32 v[124:125], v[124:125], v[116:117], v[124:125]
	v_pk_fma_f32 v[116:117], v[116:117], v[120:121], v[120:121]
	v_pk_fma_f32 v[126:127], v[126:127], v[118:119], v[126:127]
	v_pk_fma_f32 v[118:119], v[118:119], v[122:123], v[122:123]
	v_rcp_f32_e32 v116, v116
	v_rcp_f32_e32 v117, v117
	v_rcp_f32_e32 v118, v118
	v_rcp_f32_e32 v119, v119
	s_waitcnt lgkmcnt(3)
	v_pk_fma_f32 v[124:125], v[172:173], v[120:121], v[124:125]
	v_pk_fma_f32 v[126:127], v[174:175], v[122:123], v[126:127]
	v_pk_mul_f32 v[116:117], v[116:117], v[124:125]
	v_pk_mul_f32 v[118:119], v[118:119], v[126:127]
	global_store_dwordx4 v[176:177], v[116:119], off nt
	s_nop 1
	v_pk_mul_f32 v[116:117], v[116:117], s[96:97] op_sel_hi:[1,0]
	v_pk_mul_f32 v[118:119], v[118:119], s[96:97] op_sel_hi:[1,0]
	v_exp_f32_e32 v112, v112
	v_exp_f32_e32 v113, v113
	v_exp_f32_e32 v114, v114
	v_pk_fma_f32 v[112:113], v[112:113], s[98:99], s[98:99] op_sel_hi:[1,0,0]
	v_exp_f32_e32 v115, v115
	v_exp_f32_e32 v116, v116
	v_pk_fma_f32 v[114:115], v[114:115], s[98:99], s[98:99] op_sel_hi:[1,0,0]
	v_exp_f32_e32 v117, v117
	v_exp_f32_e32 v118, v118
	v_pk_fma_f32 v[112:113], v[116:117], v[112:113], v[112:113]
	v_exp_f32_e32 v119, v119
	v_pk_add_f32 v[116:117], v[116:117], 1.0 op_sel_hi:[1,0] neg_lo:[1,0] neg_hi:[1,0]
	v_rcp_f32_e32 v112, v112
	v_rcp_f32_e32 v113, v113
	v_pk_fma_f32 v[114:115], v[118:119], v[114:115], v[114:115]
	v_pk_add_f32 v[118:119], v[118:119], 1.0 op_sel_hi:[1,0] neg_lo:[1,0] neg_hi:[1,0]
	v_rcp_f32_e32 v114, v114
	v_rcp_f32_e32 v115, v115
	v_pk_mul_f32 v[112:113], v[112:113], v[116:117]
	v_pk_mul_f32 v[114:115], v[114:115], v[118:119]
	v_cvt_pk_fp8_f32 v124, v112, v113
	s_add_u32 s0, s8, s27
	s_addc_u32 s1, s9, 0
	s_ashr_i32 s35, s34, 31
	s_lshl_b64 s[34:35], s[34:35], 21
	v_ashrrev_i32_e32 v209, 31, v208
	s_add_u32 s36, s73, s34
	v_lshrrev_b32_e32 v126, 4, v210
	v_and_b32_e32 v127, 15, v210
	v_lshl_or_b32 v126, v126, 8, v127
	v_and_b32_e32 v127, 15, v208
	v_mul_u32_u24_e32 v127, 0x3f0, v127
	v_sub_u32_e32 v126, v126, v127
	v_ashrrev_i32_e32 v127, 31, v126
	v_lshl_add_u64 v[122:123], s[0:1], 0, v[126:127]
	v_cvt_pk_fp8_f32 v124, v114, v115 op_sel:[0,0,1]
	v_lshlrev_b64 v[116:117], 10, v[208:209]
	s_addc_u32 s37, s74, s35
	v_lshl_add_u64 v[118:119], v[122:123], 0, v[116:117]
	global_store_dword v[118:119], v124, off
	s_cmp_eq_u32 s30, 7
	s_cselect_b64 s[34:35], -1, 0
	s_cmp_lg_u32 s30, 7
	v_lshrrev_b32_e32 v126, 4, v210
	v_lshlrev_b32_e32 v126, 9, v126
	v_and_b32_e32 v127, 15, v210
	v_lshl_or_b32 v126, v127, 1, v126
	v_and_b32_e32 v127, 15, v208
	v_mul_u32_u24_e32 v127, 0x7e0, v127
	v_sub_u32_e32 v126, v126, v127
	v_ashrrev_i32_e32 v127, 31, v126
	v_lshl_add_u64 v[120:121], s[36:37], 0, v[126:127]
	v_pk_mul_f32 v[112:113], v[112:113], s[98:99] op_sel_hi:[1,0]
	v_pk_mul_f32 v[114:115], v[114:115], s[98:99] op_sel_hi:[1,0]
	v_cvt_pk_f16_f32 v112, v112, v113
	v_cvt_pk_f16_f32 v113, v114, v115
	v_lshl_add_u64 v[114:115], v[116:117], 1, v[120:121]
	global_store_dwordx2 v[114:115], v[112:113], off
	v_exp_f32_e32 v108, v108
	v_exp_f32_e32 v109, v109
	v_exp_f32_e32 v110, v110
	v_pk_add_f32 v[108:109], v[108:109], 1.0 op_sel_hi:[1,0]
	v_exp_f32_e32 v111, v111
	v_exp_f32_e32 v104, v104
	v_pk_add_f32 v[110:111], v[110:111], 1.0 op_sel_hi:[1,0]
	v_exp_f32_e32 v105, v105
	v_exp_f32_e32 v106, v106
	v_pk_fma_f32 v[104:105], v[104:105], v[108:109], v[108:109]
	v_exp_f32_e32 v107, v107
	v_exp_f32_e32 v100, v100
	v_pk_fma_f32 v[106:107], v[106:107], v[110:111], v[110:111]
	v_exp_f32_e32 v101, v101
	v_pk_add_f32 v[108:109], v[108:109], 2.0 op_sel_hi:[1,0] neg_lo:[1,0] neg_hi:[1,0]
	v_exp_f32_e32 v102, v102
	v_pk_add_f32 v[110:111], v[110:111], 2.0 op_sel_hi:[1,0] neg_lo:[1,0] neg_hi:[1,0]
	v_exp_f32_e32 v103, v103
	v_pk_fma_f32 v[108:109], v[108:109], v[100:101], v[108:109]
	v_pk_fma_f32 v[100:101], v[100:101], v[104:105], v[104:105]
	v_pk_fma_f32 v[110:111], v[110:111], v[102:103], v[110:111]
	v_pk_fma_f32 v[102:103], v[102:103], v[106:107], v[106:107]
	v_rcp_f32_e32 v100, v100
	v_rcp_f32_e32 v101, v101
	v_rcp_f32_e32 v102, v102
	v_rcp_f32_e32 v103, v103
	s_waitcnt lgkmcnt(2)
	v_pk_fma_f32 v[108:109], v[168:169], v[104:105], v[108:109]
	v_pk_fma_f32 v[110:111], v[170:171], v[106:107], v[110:111]
	v_lshl_add_u64 v[104:105], v[176:177], 0, s[18:19]
	v_pk_mul_f32 v[100:101], v[100:101], v[108:109]
	v_pk_mul_f32 v[102:103], v[102:103], v[110:111]
	global_store_dwordx4 v[104:105], v[100:103], off nt
	s_nop 1
	v_pk_mul_f32 v[100:101], v[100:101], s[96:97] op_sel_hi:[1,0]
	v_pk_mul_f32 v[102:103], v[102:103], s[96:97] op_sel_hi:[1,0]
	v_exp_f32_e32 v96, v96
	v_exp_f32_e32 v97, v97
	v_exp_f32_e32 v98, v98
	v_pk_fma_f32 v[96:97], v[96:97], s[98:99], s[98:99] op_sel_hi:[1,0,0]
	v_exp_f32_e32 v99, v99
	v_exp_f32_e32 v100, v100
	v_pk_fma_f32 v[98:99], v[98:99], s[98:99], s[98:99] op_sel_hi:[1,0,0]
	v_exp_f32_e32 v101, v101
	v_exp_f32_e32 v102, v102
	v_pk_fma_f32 v[96:97], v[100:101], v[96:97], v[96:97]
	v_exp_f32_e32 v103, v103
	v_pk_add_f32 v[100:101], v[100:101], 1.0 op_sel_hi:[1,0] neg_lo:[1,0] neg_hi:[1,0]
	v_rcp_f32_e32 v96, v96
	v_rcp_f32_e32 v97, v97
	v_pk_fma_f32 v[98:99], v[102:103], v[98:99], v[98:99]
	v_pk_add_f32 v[102:103], v[102:103], 1.0 op_sel_hi:[1,0] neg_lo:[1,0] neg_hi:[1,0]
	v_rcp_f32_e32 v98, v98
	v_rcp_f32_e32 v99, v99
	v_pk_mul_f32 v[96:97], v[96:97], v[100:101]
	v_pk_mul_f32 v[98:99], v[98:99], v[102:103]
	v_cvt_pk_fp8_f32 v104, v96, v97
	v_ashrrev_i32_e32 v207, 31, v206
	v_lshlrev_b64 v[100:101], 10, v[206:207]
	v_lshl_add_u64 v[102:103], v[122:123], 0, v[100:101]
	v_cvt_pk_fp8_f32 v104, v98, v99 op_sel:[0,0,1]
	v_cndmask_b32_e64 v105, 0, 1, s[34:35]
	global_store_dword v[102:103], v104, off
	v_cmp_ne_u32_e64 s[0:1], 1, v105
	v_pk_mul_f32 v[96:97], v[96:97], s[98:99] op_sel_hi:[1,0]
	v_pk_mul_f32 v[98:99], v[98:99], s[98:99] op_sel_hi:[1,0]
	v_cvt_pk_f16_f32 v96, v96, v97
	v_cvt_pk_f16_f32 v97, v98, v99
	v_lshl_add_u64 v[98:99], v[100:101], 1, v[120:121]
	global_store_dwordx2 v[98:99], v[96:97], off
	v_exp_f32_e32 v92, v92
	v_exp_f32_e32 v93, v93
	v_exp_f32_e32 v94, v94
	v_pk_add_f32 v[92:93], v[92:93], 1.0 op_sel_hi:[1,0]
	v_exp_f32_e32 v95, v95
	v_exp_f32_e32 v88, v88
	v_pk_add_f32 v[94:95], v[94:95], 1.0 op_sel_hi:[1,0]
	v_exp_f32_e32 v89, v89
	v_exp_f32_e32 v90, v90
	v_pk_fma_f32 v[88:89], v[88:89], v[92:93], v[92:93]
	v_exp_f32_e32 v91, v91
	v_exp_f32_e32 v84, v84
	v_pk_fma_f32 v[90:91], v[90:91], v[94:95], v[94:95]
	v_exp_f32_e32 v85, v85
	v_pk_add_f32 v[92:93], v[92:93], 2.0 op_sel_hi:[1,0] neg_lo:[1,0] neg_hi:[1,0]
	v_exp_f32_e32 v86, v86
	v_pk_add_f32 v[94:95], v[94:95], 2.0 op_sel_hi:[1,0] neg_lo:[1,0] neg_hi:[1,0]
	v_exp_f32_e32 v87, v87
	v_pk_fma_f32 v[92:93], v[92:93], v[84:85], v[92:93]
	v_pk_fma_f32 v[84:85], v[84:85], v[88:89], v[88:89]
	v_pk_fma_f32 v[94:95], v[94:95], v[86:87], v[94:95]
	v_pk_fma_f32 v[86:87], v[86:87], v[90:91], v[90:91]
	v_rcp_f32_e32 v84, v84
	v_rcp_f32_e32 v85, v85
	v_rcp_f32_e32 v86, v86
	v_rcp_f32_e32 v87, v87
	s_waitcnt lgkmcnt(1)
	v_pk_fma_f32 v[92:93], v[164:165], v[88:89], v[92:93]
	v_pk_fma_f32 v[94:95], v[166:167], v[90:91], v[94:95]
	v_pk_mul_f32 v[84:85], v[84:85], v[92:93]
	v_pk_mul_f32 v[86:87], v[86:87], v[94:95]
	v_lshl_add_u64 v[88:89], v[176:177], 0, s[12:13]
	global_store_dwordx4 v[88:89], v[84:87], off nt
	s_nop 1
	v_pk_mul_f32 v[84:85], v[84:85], s[96:97] op_sel_hi:[1,0]
	v_pk_mul_f32 v[86:87], v[86:87], s[96:97] op_sel_hi:[1,0]
	v_exp_f32_e32 v80, v80
	v_exp_f32_e32 v81, v81
	v_exp_f32_e32 v82, v82
	v_pk_fma_f32 v[80:81], v[80:81], s[98:99], s[98:99] op_sel_hi:[1,0,0]
	v_exp_f32_e32 v83, v83
	v_exp_f32_e32 v84, v84
	v_pk_fma_f32 v[82:83], v[82:83], s[98:99], s[98:99] op_sel_hi:[1,0,0]
	v_exp_f32_e32 v85, v85
	v_exp_f32_e32 v86, v86
	v_pk_fma_f32 v[80:81], v[84:85], v[80:81], v[80:81]
	v_exp_f32_e32 v87, v87
	v_pk_add_f32 v[84:85], v[84:85], 1.0 op_sel_hi:[1,0] neg_lo:[1,0] neg_hi:[1,0]
	v_rcp_f32_e32 v80, v80
	v_rcp_f32_e32 v81, v81
	v_pk_fma_f32 v[82:83], v[86:87], v[82:83], v[82:83]
	v_pk_add_f32 v[86:87], v[86:87], 1.0 op_sel_hi:[1,0] neg_lo:[1,0] neg_hi:[1,0]
	v_rcp_f32_e32 v82, v82
	v_rcp_f32_e32 v83, v83
	v_pk_mul_f32 v[80:81], v[80:81], v[84:85]
	v_pk_mul_f32 v[82:83], v[82:83], v[86:87]
	v_ashrrev_i32_e32 v205, 31, v204
	v_cvt_pk_fp8_f32 v88, v80, v81
	s_and_b64 vcc, exec, s[0:1]
	v_cvt_pk_fp8_f32 v88, v82, v83 op_sel:[0,0,1]
	v_lshlrev_b64 v[84:85], 10, v[204:205]
	v_lshl_add_u64 v[86:87], v[122:123], 0, v[84:85]
	global_store_dword v[86:87], v88, off
	v_pk_mul_f32 v[80:81], v[80:81], s[98:99] op_sel_hi:[1,0]
	v_pk_mul_f32 v[82:83], v[82:83], s[98:99] op_sel_hi:[1,0]
	v_cvt_pk_f16_f32 v80, v80, v81
	v_cvt_pk_f16_f32 v81, v82, v83
	v_lshl_add_u64 v[82:83], v[84:85], 1, v[120:121]
	global_store_dwordx2 v[82:83], v[80:81], off
	v_exp_f32_e32 v76, v76
	v_exp_f32_e32 v77, v77
	v_exp_f32_e32 v78, v78
	v_pk_add_f32 v[76:77], v[76:77], 1.0 op_sel_hi:[1,0]
	v_exp_f32_e32 v79, v79
	v_exp_f32_e32 v72, v72
	v_pk_add_f32 v[78:79], v[78:79], 1.0 op_sel_hi:[1,0]
	v_exp_f32_e32 v73, v73
	v_exp_f32_e32 v74, v74
	v_pk_fma_f32 v[72:73], v[72:73], v[76:77], v[76:77]
	v_exp_f32_e32 v75, v75
	v_exp_f32_e32 v68, v68
	v_pk_fma_f32 v[74:75], v[74:75], v[78:79], v[78:79]
	v_exp_f32_e32 v69, v69
	v_pk_add_f32 v[76:77], v[76:77], 2.0 op_sel_hi:[1,0] neg_lo:[1,0] neg_hi:[1,0]
	v_exp_f32_e32 v70, v70
	v_pk_add_f32 v[78:79], v[78:79], 2.0 op_sel_hi:[1,0] neg_lo:[1,0] neg_hi:[1,0]
	v_exp_f32_e32 v71, v71
	v_pk_fma_f32 v[76:77], v[76:77], v[68:69], v[76:77]
	v_pk_fma_f32 v[68:69], v[68:69], v[72:73], v[72:73]
	v_pk_fma_f32 v[78:79], v[78:79], v[70:71], v[78:79]
	v_pk_fma_f32 v[70:71], v[70:71], v[74:75], v[74:75]
	v_rcp_f32_e32 v68, v68
	v_rcp_f32_e32 v69, v69
	v_rcp_f32_e32 v70, v70
	v_rcp_f32_e32 v71, v71
	s_waitcnt lgkmcnt(0)
	v_pk_fma_f32 v[76:77], v[160:161], v[72:73], v[76:77]
	v_pk_fma_f32 v[78:79], v[162:163], v[74:75], v[78:79]
	v_lshl_add_u64 v[72:73], v[176:177], 0, s[20:21]
	v_pk_mul_f32 v[68:69], v[68:69], v[76:77]
	v_pk_mul_f32 v[70:71], v[70:71], v[78:79]
	global_store_dwordx4 v[72:73], v[68:71], off nt
	s_nop 1
	v_pk_mul_f32 v[68:69], v[68:69], s[96:97] op_sel_hi:[1,0]
	v_pk_mul_f32 v[70:71], v[70:71], s[96:97] op_sel_hi:[1,0]
	v_exp_f32_e32 v64, v64
	v_exp_f32_e32 v65, v65
	v_exp_f32_e32 v66, v66
	v_pk_fma_f32 v[64:65], v[64:65], s[98:99], s[98:99] op_sel_hi:[1,0,0]
	v_exp_f32_e32 v67, v67
	v_exp_f32_e32 v68, v68
	v_pk_fma_f32 v[66:67], v[66:67], s[98:99], s[98:99] op_sel_hi:[1,0,0]
	v_exp_f32_e32 v69, v69
	v_exp_f32_e32 v70, v70
	v_pk_fma_f32 v[64:65], v[68:69], v[64:65], v[64:65]
	v_exp_f32_e32 v71, v71
	v_pk_add_f32 v[68:69], v[68:69], 1.0 op_sel_hi:[1,0] neg_lo:[1,0] neg_hi:[1,0]
	v_rcp_f32_e32 v64, v64
	v_rcp_f32_e32 v65, v65
	v_pk_fma_f32 v[66:67], v[70:71], v[66:67], v[66:67]
	v_pk_add_f32 v[70:71], v[70:71], 1.0 op_sel_hi:[1,0] neg_lo:[1,0] neg_hi:[1,0]
	v_rcp_f32_e32 v66, v66
	v_rcp_f32_e32 v67, v67
	v_pk_mul_f32 v[64:65], v[64:65], v[68:69]
	v_pk_mul_f32 v[66:67], v[66:67], v[70:71]
	v_ashrrev_i32_e32 v203, 31, v202
	v_cvt_pk_fp8_f32 v72, v64, v65
	s_and_b64 vcc, exec, s[0:1]
	v_cvt_pk_fp8_f32 v72, v66, v67 op_sel:[0,0,1]
	v_lshlrev_b64 v[68:69], 10, v[202:203]
	v_lshl_add_u64 v[70:71], v[122:123], 0, v[68:69]
	global_store_dword v[70:71], v72, off
	v_pk_mul_f32 v[64:65], v[64:65], s[98:99] op_sel_hi:[1,0]
	v_pk_mul_f32 v[66:67], v[66:67], s[98:99] op_sel_hi:[1,0]
	v_cvt_pk_f16_f32 v64, v64, v65
	v_cvt_pk_f16_f32 v65, v66, v67
	v_lshl_add_u64 v[66:67], v[68:69], 1, v[120:121]
	global_store_dwordx2 v[66:67], v[64:65], off
	v_exp_f32_e32 v60, v60
	v_exp_f32_e32 v61, v61
	v_exp_f32_e32 v62, v62
	v_pk_add_f32 v[60:61], v[60:61], 1.0 op_sel_hi:[1,0]
	v_exp_f32_e32 v63, v63
	v_exp_f32_e32 v56, v56
	v_pk_add_f32 v[62:63], v[62:63], 1.0 op_sel_hi:[1,0]
	v_exp_f32_e32 v57, v57
	v_exp_f32_e32 v58, v58
	v_pk_fma_f32 v[56:57], v[56:57], v[60:61], v[60:61]
	v_exp_f32_e32 v59, v59
	v_exp_f32_e32 v52, v52
	v_pk_fma_f32 v[58:59], v[58:59], v[62:63], v[62:63]
	v_exp_f32_e32 v53, v53
	v_pk_add_f32 v[60:61], v[60:61], 2.0 op_sel_hi:[1,0] neg_lo:[1,0] neg_hi:[1,0]
	v_exp_f32_e32 v54, v54
	v_pk_add_f32 v[62:63], v[62:63], 2.0 op_sel_hi:[1,0] neg_lo:[1,0] neg_hi:[1,0]
	v_exp_f32_e32 v55, v55
	v_pk_fma_f32 v[60:61], v[60:61], v[52:53], v[60:61]
	v_pk_fma_f32 v[52:53], v[52:53], v[56:57], v[56:57]
	v_pk_fma_f32 v[62:63], v[62:63], v[54:55], v[62:63]
	v_pk_fma_f32 v[54:55], v[54:55], v[58:59], v[58:59]
	v_rcp_f32_e32 v52, v52
	v_rcp_f32_e32 v53, v53
	v_rcp_f32_e32 v54, v54
	v_rcp_f32_e32 v55, v55
	s_waitcnt vmcnt(8)
	v_pk_fma_f32 v[60:61], v[156:157], v[56:57], v[60:61]
	v_pk_fma_f32 v[62:63], v[158:159], v[58:59], v[62:63]
	v_pk_mul_f32 v[52:53], v[52:53], v[60:61]
	v_pk_mul_f32 v[54:55], v[54:55], v[62:63]
	v_lshl_add_u64 v[56:57], v[176:177], 0, s[14:15]
	global_store_dwordx4 v[56:57], v[52:55], off nt
	s_nop 1
	v_pk_mul_f32 v[52:53], v[52:53], s[96:97] op_sel_hi:[1,0]
	v_pk_mul_f32 v[54:55], v[54:55], s[96:97] op_sel_hi:[1,0]
	v_exp_f32_e32 v48, v48
	v_exp_f32_e32 v49, v49
	v_exp_f32_e32 v50, v50
	v_pk_fma_f32 v[48:49], v[48:49], s[98:99], s[98:99] op_sel_hi:[1,0,0]
	v_exp_f32_e32 v51, v51
	v_exp_f32_e32 v52, v52
	v_pk_fma_f32 v[50:51], v[50:51], s[98:99], s[98:99] op_sel_hi:[1,0,0]
	v_exp_f32_e32 v53, v53
	v_exp_f32_e32 v54, v54
	v_pk_fma_f32 v[48:49], v[52:53], v[48:49], v[48:49]
	v_exp_f32_e32 v55, v55
	v_pk_add_f32 v[52:53], v[52:53], 1.0 op_sel_hi:[1,0] neg_lo:[1,0] neg_hi:[1,0]
	v_rcp_f32_e32 v48, v48
	v_rcp_f32_e32 v49, v49
	v_pk_fma_f32 v[50:51], v[54:55], v[50:51], v[50:51]
	v_pk_add_f32 v[54:55], v[54:55], 1.0 op_sel_hi:[1,0] neg_lo:[1,0] neg_hi:[1,0]
	v_rcp_f32_e32 v50, v50
	v_rcp_f32_e32 v51, v51
	v_pk_mul_f32 v[48:49], v[48:49], v[52:53]
	v_pk_mul_f32 v[50:51], v[50:51], v[54:55]
	v_ashrrev_i32_e32 v201, 31, v200
	v_cvt_pk_fp8_f32 v56, v48, v49
	s_and_b64 vcc, exec, s[0:1]
	v_cvt_pk_fp8_f32 v56, v50, v51 op_sel:[0,0,1]
	v_lshlrev_b64 v[52:53], 10, v[200:201]
	v_lshl_add_u64 v[54:55], v[122:123], 0, v[52:53]
	global_store_dword v[54:55], v56, off
	v_pk_mul_f32 v[48:49], v[48:49], s[98:99] op_sel_hi:[1,0]
	v_pk_mul_f32 v[50:51], v[50:51], s[98:99] op_sel_hi:[1,0]
	v_cvt_pk_f16_f32 v48, v48, v49
	v_cvt_pk_f16_f32 v49, v50, v51
	v_lshl_add_u64 v[50:51], v[52:53], 1, v[120:121]
	global_store_dwordx2 v[50:51], v[48:49], off
	v_exp_f32_e32 v44, v44
	v_exp_f32_e32 v45, v45
	v_exp_f32_e32 v46, v46
	v_pk_add_f32 v[44:45], v[44:45], 1.0 op_sel_hi:[1,0]
	v_exp_f32_e32 v47, v47
	v_exp_f32_e32 v40, v40
	v_pk_add_f32 v[46:47], v[46:47], 1.0 op_sel_hi:[1,0]
	v_exp_f32_e32 v41, v41
	v_exp_f32_e32 v42, v42
	v_pk_fma_f32 v[40:41], v[40:41], v[44:45], v[44:45]
	v_exp_f32_e32 v43, v43
	v_exp_f32_e32 v36, v36
	v_pk_fma_f32 v[42:43], v[42:43], v[46:47], v[46:47]
	v_exp_f32_e32 v37, v37
	v_pk_add_f32 v[44:45], v[44:45], 2.0 op_sel_hi:[1,0] neg_lo:[1,0] neg_hi:[1,0]
	v_exp_f32_e32 v38, v38
	v_pk_add_f32 v[46:47], v[46:47], 2.0 op_sel_hi:[1,0] neg_lo:[1,0] neg_hi:[1,0]
	v_exp_f32_e32 v39, v39
	v_pk_fma_f32 v[44:45], v[44:45], v[36:37], v[44:45]
	v_pk_fma_f32 v[36:37], v[36:37], v[40:41], v[40:41]
	v_pk_fma_f32 v[46:47], v[46:47], v[38:39], v[46:47]
	v_pk_fma_f32 v[38:39], v[38:39], v[42:43], v[42:43]
	v_rcp_f32_e32 v36, v36
	v_rcp_f32_e32 v37, v37
	v_rcp_f32_e32 v38, v38
	v_rcp_f32_e32 v39, v39
	v_pk_fma_f32 v[44:45], v[152:153], v[40:41], v[44:45]
	v_pk_fma_f32 v[46:47], v[154:155], v[42:43], v[46:47]
	v_lshl_add_u64 v[40:41], v[176:177], 0, s[22:23]
	v_pk_mul_f32 v[36:37], v[36:37], v[44:45]
	v_pk_mul_f32 v[38:39], v[38:39], v[46:47]
	global_store_dwordx4 v[40:41], v[36:39], off nt
	s_nop 1
	v_pk_mul_f32 v[36:37], v[36:37], s[96:97] op_sel_hi:[1,0]
	v_pk_mul_f32 v[38:39], v[38:39], s[96:97] op_sel_hi:[1,0]
	v_exp_f32_e32 v32, v32
	v_exp_f32_e32 v33, v33
	v_exp_f32_e32 v34, v34
	v_pk_fma_f32 v[32:33], v[32:33], s[98:99], s[98:99] op_sel_hi:[1,0,0]
	v_exp_f32_e32 v35, v35
	v_exp_f32_e32 v36, v36
	v_pk_fma_f32 v[34:35], v[34:35], s[98:99], s[98:99] op_sel_hi:[1,0,0]
	v_exp_f32_e32 v37, v37
	v_exp_f32_e32 v38, v38
	v_pk_fma_f32 v[32:33], v[36:37], v[32:33], v[32:33]
	v_exp_f32_e32 v39, v39
	v_pk_add_f32 v[36:37], v[36:37], 1.0 op_sel_hi:[1,0] neg_lo:[1,0] neg_hi:[1,0]
	v_rcp_f32_e32 v32, v32
	v_rcp_f32_e32 v33, v33
	v_pk_fma_f32 v[34:35], v[38:39], v[34:35], v[34:35]
	v_pk_add_f32 v[38:39], v[38:39], 1.0 op_sel_hi:[1,0] neg_lo:[1,0] neg_hi:[1,0]
	v_rcp_f32_e32 v34, v34
	v_rcp_f32_e32 v35, v35
	v_pk_mul_f32 v[32:33], v[32:33], v[36:37]
	v_pk_mul_f32 v[34:35], v[34:35], v[38:39]
	v_cvt_pk_fp8_f32 v40, v32, v33
	v_or_b32_e32 v36, 16, v200
	v_ashrrev_i32_e32 v37, 31, v36
	v_lshlrev_b64 v[36:37], 10, v[36:37]
	v_cvt_pk_fp8_f32 v40, v34, v35 op_sel:[0,0,1]
	v_lshl_add_u64 v[38:39], v[122:123], 0, v[36:37]
	global_store_dword v[38:39], v40, off
	v_pk_mul_f32 v[32:33], v[32:33], s[98:99] op_sel_hi:[1,0]
	v_pk_mul_f32 v[34:35], v[34:35], s[98:99] op_sel_hi:[1,0]
	v_cvt_pk_f16_f32 v32, v32, v33
	v_cvt_pk_f16_f32 v33, v34, v35
	v_lshl_add_u64 v[34:35], v[36:37], 1, v[120:121]
	global_store_dwordx2 v[34:35], v[32:33], off
	v_exp_f32_e32 v28, v28
	v_exp_f32_e32 v29, v29
	v_exp_f32_e32 v30, v30
	v_pk_add_f32 v[28:29], v[28:29], 1.0 op_sel_hi:[1,0]
	v_exp_f32_e32 v31, v31
	v_exp_f32_e32 v24, v24
	v_pk_add_f32 v[30:31], v[30:31], 1.0 op_sel_hi:[1,0]
	v_exp_f32_e32 v25, v25
	v_exp_f32_e32 v26, v26
	v_pk_fma_f32 v[24:25], v[24:25], v[28:29], v[28:29]
	v_exp_f32_e32 v27, v27
	v_exp_f32_e32 v20, v20
	v_pk_fma_f32 v[26:27], v[26:27], v[30:31], v[30:31]
	v_exp_f32_e32 v21, v21
	v_pk_add_f32 v[28:29], v[28:29], 2.0 op_sel_hi:[1,0] neg_lo:[1,0] neg_hi:[1,0]
	v_exp_f32_e32 v22, v22
	v_pk_add_f32 v[30:31], v[30:31], 2.0 op_sel_hi:[1,0] neg_lo:[1,0] neg_hi:[1,0]
	v_exp_f32_e32 v23, v23
	v_pk_fma_f32 v[28:29], v[28:29], v[20:21], v[28:29]
	v_pk_fma_f32 v[20:21], v[20:21], v[24:25], v[24:25]
	v_pk_fma_f32 v[30:31], v[30:31], v[22:23], v[30:31]
	v_pk_fma_f32 v[22:23], v[22:23], v[26:27], v[26:27]
	v_rcp_f32_e32 v20, v20
	v_rcp_f32_e32 v21, v21
	v_rcp_f32_e32 v22, v22
	v_rcp_f32_e32 v23, v23
	v_pk_fma_f32 v[28:29], v[148:149], v[24:25], v[28:29]
	v_pk_fma_f32 v[30:31], v[150:151], v[26:27], v[30:31]
	v_pk_mul_f32 v[20:21], v[20:21], v[28:29]
	v_pk_mul_f32 v[22:23], v[22:23], v[30:31]
	v_lshl_add_u64 v[24:25], v[176:177], 0, s[16:17]
	global_store_dwordx4 v[24:25], v[20:23], off nt
	s_nop 1
	v_pk_mul_f32 v[20:21], v[20:21], s[96:97] op_sel_hi:[1,0]
	v_pk_mul_f32 v[22:23], v[22:23], s[96:97] op_sel_hi:[1,0]
	v_exp_f32_e32 v16, v16
	v_exp_f32_e32 v17, v17
	v_exp_f32_e32 v18, v18
	v_pk_fma_f32 v[16:17], v[16:17], s[98:99], s[98:99] op_sel_hi:[1,0,0]
	v_exp_f32_e32 v19, v19
	v_exp_f32_e32 v20, v20
	v_pk_fma_f32 v[18:19], v[18:19], s[98:99], s[98:99] op_sel_hi:[1,0,0]
	v_exp_f32_e32 v21, v21
	v_exp_f32_e32 v22, v22
	v_pk_fma_f32 v[16:17], v[20:21], v[16:17], v[16:17]
	v_exp_f32_e32 v23, v23
	v_pk_add_f32 v[20:21], v[20:21], 1.0 op_sel_hi:[1,0] neg_lo:[1,0] neg_hi:[1,0]
	v_rcp_f32_e32 v16, v16
	v_rcp_f32_e32 v17, v17
	v_pk_fma_f32 v[18:19], v[22:23], v[18:19], v[18:19]
	v_pk_add_f32 v[22:23], v[22:23], 1.0 op_sel_hi:[1,0] neg_lo:[1,0] neg_hi:[1,0]
	v_rcp_f32_e32 v18, v18
	v_rcp_f32_e32 v19, v19
	v_pk_mul_f32 v[16:17], v[16:17], v[20:21]
	v_pk_mul_f32 v[18:19], v[18:19], v[22:23]
	v_cvt_pk_fp8_f32 v24, v16, v17
	v_or_b32_e32 v20, 32, v200
	v_ashrrev_i32_e32 v21, 31, v20
	v_lshlrev_b64 v[20:21], 10, v[20:21]
	v_cvt_pk_fp8_f32 v24, v18, v19 op_sel:[0,0,1]
	v_lshl_add_u64 v[22:23], v[122:123], 0, v[20:21]
	global_store_dword v[22:23], v24, off
	v_pk_mul_f32 v[16:17], v[16:17], s[98:99] op_sel_hi:[1,0]
	v_pk_mul_f32 v[18:19], v[18:19], s[98:99] op_sel_hi:[1,0]
	v_cvt_pk_f16_f32 v16, v16, v17
	v_cvt_pk_f16_f32 v17, v18, v19
	v_lshl_add_u64 v[18:19], v[20:21], 1, v[120:121]
	global_store_dwordx2 v[18:19], v[16:17], off
	v_exp_f32_e32 v12, v12
	v_exp_f32_e32 v13, v13
	v_exp_f32_e32 v14, v14
	v_pk_add_f32 v[12:13], v[12:13], 1.0 op_sel_hi:[1,0]
	v_exp_f32_e32 v15, v15
	v_exp_f32_e32 v8, v8
	v_pk_add_f32 v[14:15], v[14:15], 1.0 op_sel_hi:[1,0]
	v_exp_f32_e32 v9, v9
	v_exp_f32_e32 v10, v10
	v_pk_fma_f32 v[8:9], v[8:9], v[12:13], v[12:13]
	v_exp_f32_e32 v11, v11
	v_exp_f32_e32 v4, v4
	v_pk_fma_f32 v[10:11], v[10:11], v[14:15], v[14:15]
	v_exp_f32_e32 v5, v5
	v_pk_add_f32 v[12:13], v[12:13], 2.0 op_sel_hi:[1,0] neg_lo:[1,0] neg_hi:[1,0]
	v_exp_f32_e32 v6, v6
	v_pk_add_f32 v[14:15], v[14:15], 2.0 op_sel_hi:[1,0] neg_lo:[1,0] neg_hi:[1,0]
	v_exp_f32_e32 v7, v7
	v_pk_fma_f32 v[12:13], v[12:13], v[4:5], v[12:13]
	v_pk_fma_f32 v[4:5], v[4:5], v[8:9], v[8:9]
	v_pk_fma_f32 v[14:15], v[14:15], v[6:7], v[14:15]
	v_pk_fma_f32 v[6:7], v[6:7], v[10:11], v[10:11]
	v_rcp_f32_e32 v4, v4
	v_rcp_f32_e32 v5, v5
	v_rcp_f32_e32 v6, v6
	v_rcp_f32_e32 v7, v7
	v_pk_fma_f32 v[12:13], v[144:145], v[8:9], v[12:13]
	v_pk_fma_f32 v[14:15], v[146:147], v[10:11], v[14:15]
	v_lshl_add_u64 v[8:9], v[176:177], 0, s[24:25]
	v_pk_mul_f32 v[4:5], v[4:5], v[12:13]
	v_pk_mul_f32 v[6:7], v[6:7], v[14:15]
	global_store_dwordx4 v[8:9], v[4:7], off nt
	s_nop 1
	v_pk_mul_f32 v[4:5], v[4:5], s[96:97] op_sel_hi:[1,0]
	v_pk_mul_f32 v[6:7], v[6:7], s[96:97] op_sel_hi:[1,0]
	v_exp_f32_e32 v0, v0
	v_exp_f32_e32 v1, v1
	v_exp_f32_e32 v2, v2
	v_pk_fma_f32 v[0:1], v[0:1], s[98:99], s[98:99] op_sel_hi:[1,0,0]
	v_exp_f32_e32 v3, v3
	v_exp_f32_e32 v4, v4
	v_pk_fma_f32 v[2:3], v[2:3], s[98:99], s[98:99] op_sel_hi:[1,0,0]
	v_exp_f32_e32 v5, v5
	v_exp_f32_e32 v6, v6
	v_pk_fma_f32 v[0:1], v[4:5], v[0:1], v[0:1]
	v_exp_f32_e32 v7, v7
	v_pk_add_f32 v[4:5], v[4:5], 1.0 op_sel_hi:[1,0] neg_lo:[1,0] neg_hi:[1,0]
	v_rcp_f32_e32 v0, v0
	v_rcp_f32_e32 v1, v1
	v_pk_fma_f32 v[2:3], v[6:7], v[2:3], v[2:3]
	v_pk_add_f32 v[6:7], v[6:7], 1.0 op_sel_hi:[1,0] neg_lo:[1,0] neg_hi:[1,0]
	v_rcp_f32_e32 v2, v2
	v_rcp_f32_e32 v3, v3
	v_pk_mul_f32 v[0:1], v[0:1], v[4:5]
	v_pk_mul_f32 v[2:3], v[2:3], v[6:7]
	v_cvt_pk_fp8_f32 v8, v0, v1
	v_or_b32_e32 v4, 48, v200
	v_ashrrev_i32_e32 v5, 31, v4
	v_lshlrev_b64 v[4:5], 10, v[4:5]
	v_cvt_pk_fp8_f32 v8, v2, v3 op_sel:[0,0,1]
	v_lshl_add_u64 v[6:7], v[122:123], 0, v[4:5]
	global_store_dword v[6:7], v8, off
	v_pk_mul_f32 v[0:1], v[0:1], s[98:99] op_sel_hi:[1,0]
	v_pk_mul_f32 v[2:3], v[2:3], s[98:99] op_sel_hi:[1,0]
	v_cvt_pk_f16_f32 v0, v0, v1
	v_cvt_pk_f16_f32 v1, v2, v3
	v_lshl_add_u64 v[2:3], v[4:5], 1, v[120:121]
	global_store_dwordx2 v[2:3], v[0:1], off
	s_branch .LBB2_24
.Lmy_epi_last:
	s_cmp_eq_u32 s30, 7
	s_cbranch_scc1 .Lmy_epi_l7
	v_exp_f32_e32 v124, v124
	v_exp_f32_e32 v125, v125
	v_exp_f32_e32 v126, v126
	v_pk_add_f32 v[124:125], v[124:125], 1.0 op_sel_hi:[1,0]
	v_exp_f32_e32 v127, v127
	v_exp_f32_e32 v120, v120
	v_pk_add_f32 v[126:127], v[126:127], 1.0 op_sel_hi:[1,0]
	v_exp_f32_e32 v121, v121
	v_exp_f32_e32 v122, v122
	v_pk_fma_f32 v[120:121], v[120:121], v[124:125], v[124:125]
	v_exp_f32_e32 v123, v123
	v_exp_f32_e32 v116, v116
	v_pk_fma_f32 v[122:123], v[122:123], v[126:127], v[126:127]
	v_exp_f32_e32 v117, v117
	v_pk_add_f32 v[124:125], v[124:125], 2.0 op_sel_hi:[1,0] neg_lo:[1,0] neg_hi:[1,0]
	v_exp_f32_e32 v118, v118
	v_pk_add_f32 v[126:127], v[126:127], 2.0 op_sel_hi:[1,0] neg_lo:[1,0] neg_hi:[1,0]
	v_exp_f32_e32 v119, v119
	v_pk_fma_f32 v[124:125], v[124:125], v[116:117], v[124:125]
	v_pk_fma_f32 v[116:117], v[116:117], v[120:121], v[120:121]
	v_pk_fma_f32 v[126:127], v[126:127], v[118:119], v[126:127]
	v_pk_fma_f32 v[118:119], v[118:119], v[122:123], v[122:123]
	v_rcp_f32_e32 v116, v116
	v_rcp_f32_e32 v117, v117
	v_rcp_f32_e32 v118, v118
	v_rcp_f32_e32 v119, v119
	s_waitcnt lgkmcnt(3)
	v_pk_fma_f32 v[124:125], v[172:173], v[120:121], v[124:125]
	v_pk_fma_f32 v[126:127], v[174:175], v[122:123], v[126:127]
	v_pk_mul_f32 v[116:117], v[116:117], v[124:125]
	v_pk_mul_f32 v[118:119], v[118:119], v[126:127]
	global_store_dwordx4 v[176:177], v[116:119], off sc1
	s_nop 1
	v_pk_mul_f32 v[116:117], v[116:117], s[96:97] op_sel_hi:[1,0]
	v_pk_mul_f32 v[118:119], v[118:119], s[96:97] op_sel_hi:[1,0]
	v_exp_f32_e32 v112, v112
	v_exp_f32_e32 v113, v113
	v_exp_f32_e32 v114, v114
	v_pk_fma_f32 v[112:113], v[112:113], s[98:99], s[98:99] op_sel_hi:[1,0,0]
	v_exp_f32_e32 v115, v115
	v_exp_f32_e32 v116, v116
	v_pk_fma_f32 v[114:115], v[114:115], s[98:99], s[98:99] op_sel_hi:[1,0,0]
	v_exp_f32_e32 v117, v117
	v_exp_f32_e32 v118, v118
	v_pk_fma_f32 v[112:113], v[116:117], v[112:113], v[112:113]
	v_exp_f32_e32 v119, v119
	v_pk_add_f32 v[116:117], v[116:117], 1.0 op_sel_hi:[1,0] neg_lo:[1,0] neg_hi:[1,0]
	v_rcp_f32_e32 v112, v112
	v_rcp_f32_e32 v113, v113
	v_pk_fma_f32 v[114:115], v[118:119], v[114:115], v[114:115]
	v_pk_add_f32 v[118:119], v[118:119], 1.0 op_sel_hi:[1,0] neg_lo:[1,0] neg_hi:[1,0]
	v_rcp_f32_e32 v114, v114
	v_rcp_f32_e32 v115, v115
	v_pk_mul_f32 v[112:113], v[112:113], v[116:117]
	v_pk_mul_f32 v[114:115], v[114:115], v[118:119]
	v_cvt_pk_fp8_f32 v124, v112, v113
	s_add_u32 s0, s8, s27
	s_addc_u32 s1, s9, 0
	s_ashr_i32 s35, s34, 31
	s_lshl_b64 s[34:35], s[34:35], 21
	v_ashrrev_i32_e32 v209, 31, v208
	s_add_u32 s36, s73, s34
	v_lshrrev_b32_e32 v126, 4, v210
	v_and_b32_e32 v127, 15, v210
	v_lshl_or_b32 v126, v126, 8, v127
	v_and_b32_e32 v127, 15, v208
	v_mul_u32_u24_e32 v127, 0x3f0, v127
	v_sub_u32_e32 v126, v126, v127
	v_ashrrev_i32_e32 v127, 31, v126
	v_lshl_add_u64 v[122:123], s[0:1], 0, v[126:127]
	v_cvt_pk_fp8_f32 v124, v114, v115 op_sel:[0,0,1]
	v_lshlrev_b64 v[116:117], 10, v[208:209]
	s_addc_u32 s37, s74, s35
	v_lshl_add_u64 v[118:119], v[122:123], 0, v[116:117]
	global_store_dword v[118:119], v124, off sc1
	s_cmp_eq_u32 s30, 7
	s_cselect_b64 s[34:35], -1, 0
	s_cmp_lg_u32 s30, 7
	v_lshrrev_b32_e32 v126, 4, v210
	v_lshlrev_b32_e32 v126, 9, v126
	v_and_b32_e32 v127, 15, v210
	v_lshl_or_b32 v126, v127, 1, v126
	v_and_b32_e32 v127, 15, v208
	v_mul_u32_u24_e32 v127, 0x7e0, v127
	v_sub_u32_e32 v126, v126, v127
	v_ashrrev_i32_e32 v127, 31, v126
	v_lshl_add_u64 v[120:121], s[36:37], 0, v[126:127]
	v_exp_f32_e32 v108, v108
	v_exp_f32_e32 v109, v109
	v_exp_f32_e32 v110, v110
	v_pk_add_f32 v[108:109], v[108:109], 1.0 op_sel_hi:[1,0]
	v_exp_f32_e32 v111, v111
	v_exp_f32_e32 v104, v104
	v_pk_add_f32 v[110:111], v[110:111], 1.0 op_sel_hi:[1,0]
	v_exp_f32_e32 v105, v105
	v_exp_f32_e32 v106, v106
	v_pk_fma_f32 v[104:105], v[104:105], v[108:109], v[108:109]
	v_exp_f32_e32 v107, v107
	v_exp_f32_e32 v100, v100
	v_pk_fma_f32 v[106:107], v[106:107], v[110:111], v[110:111]
	v_exp_f32_e32 v101, v101
	v_pk_add_f32 v[108:109], v[108:109], 2.0 op_sel_hi:[1,0] neg_lo:[1,0] neg_hi:[1,0]
	v_exp_f32_e32 v102, v102
	v_pk_add_f32 v[110:111], v[110:111], 2.0 op_sel_hi:[1,0] neg_lo:[1,0] neg_hi:[1,0]
	v_exp_f32_e32 v103, v103
	v_pk_fma_f32 v[108:109], v[108:109], v[100:101], v[108:109]
	v_pk_fma_f32 v[100:101], v[100:101], v[104:105], v[104:105]
	v_pk_fma_f32 v[110:111], v[110:111], v[102:103], v[110:111]
	v_pk_fma_f32 v[102:103], v[102:103], v[106:107], v[106:107]
	v_rcp_f32_e32 v100, v100
	v_rcp_f32_e32 v101, v101
	v_rcp_f32_e32 v102, v102
	v_rcp_f32_e32 v103, v103
	s_waitcnt lgkmcnt(2)
	v_pk_fma_f32 v[108:109], v[168:169], v[104:105], v[108:109]
	v_pk_fma_f32 v[110:111], v[170:171], v[106:107], v[110:111]
	v_lshl_add_u64 v[104:105], v[176:177], 0, s[18:19]
	v_pk_mul_f32 v[100:101], v[100:101], v[108:109]
	v_pk_mul_f32 v[102:103], v[102:103], v[110:111]
	global_store_dwordx4 v[104:105], v[100:103], off sc1
	s_nop 1
	v_pk_mul_f32 v[100:101], v[100:101], s[96:97] op_sel_hi:[1,0]
	v_pk_mul_f32 v[102:103], v[102:103], s[96:97] op_sel_hi:[1,0]
	v_exp_f32_e32 v96, v96
	v_exp_f32_e32 v97, v97
	v_exp_f32_e32 v98, v98
	v_pk_fma_f32 v[96:97], v[96:97], s[98:99], s[98:99] op_sel_hi:[1,0,0]
	v_exp_f32_e32 v99, v99
	v_exp_f32_e32 v100, v100
	v_pk_fma_f32 v[98:99], v[98:99], s[98:99], s[98:99] op_sel_hi:[1,0,0]
	v_exp_f32_e32 v101, v101
	v_exp_f32_e32 v102, v102
	v_pk_fma_f32 v[96:97], v[100:101], v[96:97], v[96:97]
	v_exp_f32_e32 v103, v103
	v_pk_add_f32 v[100:101], v[100:101], 1.0 op_sel_hi:[1,0] neg_lo:[1,0] neg_hi:[1,0]
	v_rcp_f32_e32 v96, v96
	v_rcp_f32_e32 v97, v97
	v_pk_fma_f32 v[98:99], v[102:103], v[98:99], v[98:99]
	v_pk_add_f32 v[102:103], v[102:103], 1.0 op_sel_hi:[1,0] neg_lo:[1,0] neg_hi:[1,0]
	v_rcp_f32_e32 v98, v98
	v_rcp_f32_e32 v99, v99
	v_pk_mul_f32 v[96:97], v[96:97], v[100:101]
	v_pk_mul_f32 v[98:99], v[98:99], v[102:103]
	v_cvt_pk_fp8_f32 v104, v96, v97
	v_ashrrev_i32_e32 v207, 31, v206
	v_lshlrev_b64 v[100:101], 10, v[206:207]
	v_lshl_add_u64 v[102:103], v[122:123], 0, v[100:101]
	v_cvt_pk_fp8_f32 v104, v98, v99 op_sel:[0,0,1]
	v_cndmask_b32_e64 v105, 0, 1, s[34:35]
	global_store_dword v[102:103], v104, off sc1
	v_cmp_ne_u32_e64 s[0:1], 1, v105
	v_exp_f32_e32 v92, v92
	v_exp_f32_e32 v93, v93
	v_exp_f32_e32 v94, v94
	v_pk_add_f32 v[92:93], v[92:93], 1.0 op_sel_hi:[1,0]
	v_exp_f32_e32 v95, v95
	v_exp_f32_e32 v88, v88
	v_pk_add_f32 v[94:95], v[94:95], 1.0 op_sel_hi:[1,0]
	v_exp_f32_e32 v89, v89
	v_exp_f32_e32 v90, v90
	v_pk_fma_f32 v[88:89], v[88:89], v[92:93], v[92:93]
	v_exp_f32_e32 v91, v91
	v_exp_f32_e32 v84, v84
	v_pk_fma_f32 v[90:91], v[90:91], v[94:95], v[94:95]
	v_exp_f32_e32 v85, v85
	v_pk_add_f32 v[92:93], v[92:93], 2.0 op_sel_hi:[1,0] neg_lo:[1,0] neg_hi:[1,0]
	v_exp_f32_e32 v86, v86
	v_pk_add_f32 v[94:95], v[94:95], 2.0 op_sel_hi:[1,0] neg_lo:[1,0] neg_hi:[1,0]
	v_exp_f32_e32 v87, v87
	v_pk_fma_f32 v[92:93], v[92:93], v[84:85], v[92:93]
	v_pk_fma_f32 v[84:85], v[84:85], v[88:89], v[88:89]
	v_pk_fma_f32 v[94:95], v[94:95], v[86:87], v[94:95]
	v_pk_fma_f32 v[86:87], v[86:87], v[90:91], v[90:91]
	v_rcp_f32_e32 v84, v84
	v_rcp_f32_e32 v85, v85
	v_rcp_f32_e32 v86, v86
	v_rcp_f32_e32 v87, v87
	s_waitcnt lgkmcnt(1)
	v_pk_fma_f32 v[92:93], v[164:165], v[88:89], v[92:93]
	v_pk_fma_f32 v[94:95], v[166:167], v[90:91], v[94:95]
	v_pk_mul_f32 v[84:85], v[84:85], v[92:93]
	v_pk_mul_f32 v[86:87], v[86:87], v[94:95]
	v_lshl_add_u64 v[88:89], v[176:177], 0, s[12:13]
	global_store_dwordx4 v[88:89], v[84:87], off sc1
	s_nop 1
	v_pk_mul_f32 v[84:85], v[84:85], s[96:97] op_sel_hi:[1,0]
	v_pk_mul_f32 v[86:87], v[86:87], s[96:97] op_sel_hi:[1,0]
	v_exp_f32_e32 v80, v80
	v_exp_f32_e32 v81, v81
	v_exp_f32_e32 v82, v82
	v_pk_fma_f32 v[80:81], v[80:81], s[98:99], s[98:99] op_sel_hi:[1,0,0]
	v_exp_f32_e32 v83, v83
	v_exp_f32_e32 v84, v84
	v_pk_fma_f32 v[82:83], v[82:83], s[98:99], s[98:99] op_sel_hi:[1,0,0]
	v_exp_f32_e32 v85, v85
	v_exp_f32_e32 v86, v86
	v_pk_fma_f32 v[80:81], v[84:85], v[80:81], v[80:81]
	v_exp_f32_e32 v87, v87
	v_pk_add_f32 v[84:85], v[84:85], 1.0 op_sel_hi:[1,0] neg_lo:[1,0] neg_hi:[1,0]
	v_rcp_f32_e32 v80, v80
	v_rcp_f32_e32 v81, v81
	v_pk_fma_f32 v[82:83], v[86:87], v[82:83], v[82:83]
	v_pk_add_f32 v[86:87], v[86:87], 1.0 op_sel_hi:[1,0] neg_lo:[1,0] neg_hi:[1,0]
	v_rcp_f32_e32 v82, v82
	v_rcp_f32_e32 v83, v83
	v_pk_mul_f32 v[80:81], v[80:81], v[84:85]
	v_pk_mul_f32 v[82:83], v[82:83], v[86:87]
	v_ashrrev_i32_e32 v205, 31, v204
	v_cvt_pk_fp8_f32 v88, v80, v81
	s_and_b64 vcc, exec, s[0:1]
	v_cvt_pk_fp8_f32 v88, v82, v83 op_sel:[0,0,1]
	v_lshlrev_b64 v[84:85], 10, v[204:205]
	v_lshl_add_u64 v[86:87], v[122:123], 0, v[84:85]
	global_store_dword v[86:87], v88, off sc1
	v_exp_f32_e32 v76, v76
	v_exp_f32_e32 v77, v77
	v_exp_f32_e32 v78, v78
	v_pk_add_f32 v[76:77], v[76:77], 1.0 op_sel_hi:[1,0]
	v_exp_f32_e32 v79, v79
	v_exp_f32_e32 v72, v72
	v_pk_add_f32 v[78:79], v[78:79], 1.0 op_sel_hi:[1,0]
	v_exp_f32_e32 v73, v73
	v_exp_f32_e32 v74, v74
	v_pk_fma_f32 v[72:73], v[72:73], v[76:77], v[76:77]
	v_exp_f32_e32 v75, v75
	v_exp_f32_e32 v68, v68
	v_pk_fma_f32 v[74:75], v[74:75], v[78:79], v[78:79]
	v_exp_f32_e32 v69, v69
	v_pk_add_f32 v[76:77], v[76:77], 2.0 op_sel_hi:[1,0] neg_lo:[1,0] neg_hi:[1,0]
	v_exp_f32_e32 v70, v70
	v_pk_add_f32 v[78:79], v[78:79], 2.0 op_sel_hi:[1,0] neg_lo:[1,0] neg_hi:[1,0]
	v_exp_f32_e32 v71, v71
	v_pk_fma_f32 v[76:77], v[76:77], v[68:69], v[76:77]
	v_pk_fma_f32 v[68:69], v[68:69], v[72:73], v[72:73]
	v_pk_fma_f32 v[78:79], v[78:79], v[70:71], v[78:79]
	v_pk_fma_f32 v[70:71], v[70:71], v[74:75], v[74:75]
	v_rcp_f32_e32 v68, v68
	v_rcp_f32_e32 v69, v69
	v_rcp_f32_e32 v70, v70
	v_rcp_f32_e32 v71, v71
	s_waitcnt lgkmcnt(0)
	v_pk_fma_f32 v[76:77], v[160:161], v[72:73], v[76:77]
	v_pk_fma_f32 v[78:79], v[162:163], v[74:75], v[78:79]
	v_lshl_add_u64 v[72:73], v[176:177], 0, s[20:21]
	v_pk_mul_f32 v[68:69], v[68:69], v[76:77]
	v_pk_mul_f32 v[70:71], v[70:71], v[78:79]
	global_store_dwordx4 v[72:73], v[68:71], off sc1
	s_nop 1
	v_pk_mul_f32 v[68:69], v[68:69], s[96:97] op_sel_hi:[1,0]
	v_pk_mul_f32 v[70:71], v[70:71], s[96:97] op_sel_hi:[1,0]
	v_exp_f32_e32 v64, v64
	v_exp_f32_e32 v65, v65
	v_exp_f32_e32 v66, v66
	v_pk_fma_f32 v[64:65], v[64:65], s[98:99], s[98:99] op_sel_hi:[1,0,0]
	v_exp_f32_e32 v67, v67
	v_exp_f32_e32 v68, v68
	v_pk_fma_f32 v[66:67], v[66:67], s[98:99], s[98:99] op_sel_hi:[1,0,0]
	v_exp_f32_e32 v69, v69
	v_exp_f32_e32 v70, v70
	v_pk_fma_f32 v[64:65], v[68:69], v[64:65], v[64:65]
	v_exp_f32_e32 v71, v71
	v_pk_add_f32 v[68:69], v[68:69], 1.0 op_sel_hi:[1,0] neg_lo:[1,0] neg_hi:[1,0]
	v_rcp_f32_e32 v64, v64
	v_rcp_f32_e32 v65, v65
	v_pk_fma_f32 v[66:67], v[70:71], v[66:67], v[66:67]
	v_pk_add_f32 v[70:71], v[70:71], 1.0 op_sel_hi:[1,0] neg_lo:[1,0] neg_hi:[1,0]
	v_rcp_f32_e32 v66, v66
	v_rcp_f32_e32 v67, v67
	v_pk_mul_f32 v[64:65], v[64:65], v[68:69]
	v_pk_mul_f32 v[66:67], v[66:67], v[70:71]
	v_ashrrev_i32_e32 v203, 31, v202
	v_cvt_pk_fp8_f32 v72, v64, v65
	s_and_b64 vcc, exec, s[0:1]
	v_cvt_pk_fp8_f32 v72, v66, v67 op_sel:[0,0,1]
	v_lshlrev_b64 v[68:69], 10, v[202:203]
	v_lshl_add_u64 v[70:71], v[122:123], 0, v[68:69]
	global_store_dword v[70:71], v72, off sc1
	v_exp_f32_e32 v60, v60
	v_exp_f32_e32 v61, v61
	v_exp_f32_e32 v62, v62
	v_pk_add_f32 v[60:61], v[60:61], 1.0 op_sel_hi:[1,0]
	v_exp_f32_e32 v63, v63
	v_exp_f32_e32 v56, v56
	v_pk_add_f32 v[62:63], v[62:63], 1.0 op_sel_hi:[1,0]
	v_exp_f32_e32 v57, v57
	v_exp_f32_e32 v58, v58
	v_pk_fma_f32 v[56:57], v[56:57], v[60:61], v[60:61]
	v_exp_f32_e32 v59, v59
	v_exp_f32_e32 v52, v52
	v_pk_fma_f32 v[58:59], v[58:59], v[62:63], v[62:63]
	v_exp_f32_e32 v53, v53
	v_pk_add_f32 v[60:61], v[60:61], 2.0 op_sel_hi:[1,0] neg_lo:[1,0] neg_hi:[1,0]
	v_exp_f32_e32 v54, v54
	v_pk_add_f32 v[62:63], v[62:63], 2.0 op_sel_hi:[1,0] neg_lo:[1,0] neg_hi:[1,0]
	v_exp_f32_e32 v55, v55
	v_pk_fma_f32 v[60:61], v[60:61], v[52:53], v[60:61]
	v_pk_fma_f32 v[52:53], v[52:53], v[56:57], v[56:57]
	v_pk_fma_f32 v[62:63], v[62:63], v[54:55], v[62:63]
	v_pk_fma_f32 v[54:55], v[54:55], v[58:59], v[58:59]
	v_rcp_f32_e32 v52, v52
	v_rcp_f32_e32 v53, v53
	v_rcp_f32_e32 v54, v54
	v_rcp_f32_e32 v55, v55
	s_waitcnt vmcnt(8)
	v_pk_fma_f32 v[60:61], v[156:157], v[56:57], v[60:61]
	v_pk_fma_f32 v[62:63], v[158:159], v[58:59], v[62:63]
	v_pk_mul_f32 v[52:53], v[52:53], v[60:61]
	v_pk_mul_f32 v[54:55], v[54:55], v[62:63]
	v_lshl_add_u64 v[56:57], v[176:177], 0, s[14:15]
	global_store_dwordx4 v[56:57], v[52:55], off sc1
	s_nop 1
	v_pk_mul_f32 v[52:53], v[52:53], s[96:97] op_sel_hi:[1,0]
	v_pk_mul_f32 v[54:55], v[54:55], s[96:97] op_sel_hi:[1,0]
	v_exp_f32_e32 v48, v48
	v_exp_f32_e32 v49, v49
	v_exp_f32_e32 v50, v50
	v_pk_fma_f32 v[48:49], v[48:49], s[98:99], s[98:99] op_sel_hi:[1,0,0]
	v_exp_f32_e32 v51, v51
	v_exp_f32_e32 v52, v52
	v_pk_fma_f32 v[50:51], v[50:51], s[98:99], s[98:99] op_sel_hi:[1,0,0]
	v_exp_f32_e32 v53, v53
	v_exp_f32_e32 v54, v54
	v_pk_fma_f32 v[48:49], v[52:53], v[48:49], v[48:49]
	v_exp_f32_e32 v55, v55
	v_pk_add_f32 v[52:53], v[52:53], 1.0 op_sel_hi:[1,0] neg_lo:[1,0] neg_hi:[1,0]
	v_rcp_f32_e32 v48, v48
	v_rcp_f32_e32 v49, v49
	v_pk_fma_f32 v[50:51], v[54:55], v[50:51], v[50:51]
	v_pk_add_f32 v[54:55], v[54:55], 1.0 op_sel_hi:[1,0] neg_lo:[1,0] neg_hi:[1,0]
	v_rcp_f32_e32 v50, v50
	v_rcp_f32_e32 v51, v51
	v_pk_mul_f32 v[48:49], v[48:49], v[52:53]
	v_pk_mul_f32 v[50:51], v[50:51], v[54:55]
	v_ashrrev_i32_e32 v201, 31, v200
	v_cvt_pk_fp8_f32 v56, v48, v49
	s_and_b64 vcc, exec, s[0:1]
	v_cvt_pk_fp8_f32 v56, v50, v51 op_sel:[0,0,1]
	v_lshlrev_b64 v[52:53], 10, v[200:201]
	v_lshl_add_u64 v[54:55], v[122:123], 0, v[52:53]
	global_store_dword v[54:55], v56, off sc1
	v_exp_f32_e32 v44, v44
	v_exp_f32_e32 v45, v45
	v_exp_f32_e32 v46, v46
	v_pk_add_f32 v[44:45], v[44:45], 1.0 op_sel_hi:[1,0]
	v_exp_f32_e32 v47, v47
	v_exp_f32_e32 v40, v40
	v_pk_add_f32 v[46:47], v[46:47], 1.0 op_sel_hi:[1,0]
	v_exp_f32_e32 v41, v41
	v_exp_f32_e32 v42, v42
	v_pk_fma_f32 v[40:41], v[40:41], v[44:45], v[44:45]
	v_exp_f32_e32 v43, v43
	v_exp_f32_e32 v36, v36
	v_pk_fma_f32 v[42:43], v[42:43], v[46:47], v[46:47]
	v_exp_f32_e32 v37, v37
	v_pk_add_f32 v[44:45], v[44:45], 2.0 op_sel_hi:[1,0] neg_lo:[1,0] neg_hi:[1,0]
	v_exp_f32_e32 v38, v38
	v_pk_add_f32 v[46:47], v[46:47], 2.0 op_sel_hi:[1,0] neg_lo:[1,0] neg_hi:[1,0]
	v_exp_f32_e32 v39, v39
	v_pk_fma_f32 v[44:45], v[44:45], v[36:37], v[44:45]
	v_pk_fma_f32 v[36:37], v[36:37], v[40:41], v[40:41]
	v_pk_fma_f32 v[46:47], v[46:47], v[38:39], v[46:47]
	v_pk_fma_f32 v[38:39], v[38:39], v[42:43], v[42:43]
	v_rcp_f32_e32 v36, v36
	v_rcp_f32_e32 v37, v37
	v_rcp_f32_e32 v38, v38
	v_rcp_f32_e32 v39, v39
	v_pk_fma_f32 v[44:45], v[152:153], v[40:41], v[44:45]
	v_pk_fma_f32 v[46:47], v[154:155], v[42:43], v[46:47]
	v_lshl_add_u64 v[40:41], v[176:177], 0, s[22:23]
	v_pk_mul_f32 v[36:37], v[36:37], v[44:45]
	v_pk_mul_f32 v[38:39], v[38:39], v[46:47]
	global_store_dwordx4 v[40:41], v[36:39], off sc1
	s_nop 1
	v_pk_mul_f32 v[36:37], v[36:37], s[96:97] op_sel_hi:[1,0]
	v_pk_mul_f32 v[38:39], v[38:39], s[96:97] op_sel_hi:[1,0]
	v_exp_f32_e32 v32, v32
	v_exp_f32_e32 v33, v33
	v_exp_f32_e32 v34, v34
	v_pk_fma_f32 v[32:33], v[32:33], s[98:99], s[98:99] op_sel_hi:[1,0,0]
	v_exp_f32_e32 v35, v35
	v_exp_f32_e32 v36, v36
	v_pk_fma_f32 v[34:35], v[34:35], s[98:99], s[98:99] op_sel_hi:[1,0,0]
	v_exp_f32_e32 v37, v37
	v_exp_f32_e32 v38, v38
	v_pk_fma_f32 v[32:33], v[36:37], v[32:33], v[32:33]
	v_exp_f32_e32 v39, v39
	v_pk_add_f32 v[36:37], v[36:37], 1.0 op_sel_hi:[1,0] neg_lo:[1,0] neg_hi:[1,0]
	v_rcp_f32_e32 v32, v32
	v_rcp_f32_e32 v33, v33
	v_pk_fma_f32 v[34:35], v[38:39], v[34:35], v[34:35]
	v_pk_add_f32 v[38:39], v[38:39], 1.0 op_sel_hi:[1,0] neg_lo:[1,0] neg_hi:[1,0]
	v_rcp_f32_e32 v34, v34
	v_rcp_f32_e32 v35, v35
	v_pk_mul_f32 v[32:33], v[32:33], v[36:37]
	v_pk_mul_f32 v[34:35], v[34:35], v[38:39]
	v_cvt_pk_fp8_f32 v40, v32, v33
	v_or_b32_e32 v36, 16, v200
	v_ashrrev_i32_e32 v37, 31, v36
	v_lshlrev_b64 v[36:37], 10, v[36:37]
	v_cvt_pk_fp8_f32 v40, v34, v35 op_sel:[0,0,1]
	v_lshl_add_u64 v[38:39], v[122:123], 0, v[36:37]
	global_store_dword v[38:39], v40, off sc1
	v_exp_f32_e32 v28, v28
	v_exp_f32_e32 v29, v29
	v_exp_f32_e32 v30, v30
	v_pk_add_f32 v[28:29], v[28:29], 1.0 op_sel_hi:[1,0]
	v_exp_f32_e32 v31, v31
	v_exp_f32_e32 v24, v24
	v_pk_add_f32 v[30:31], v[30:31], 1.0 op_sel_hi:[1,0]
	v_exp_f32_e32 v25, v25
	v_exp_f32_e32 v26, v26
	v_pk_fma_f32 v[24:25], v[24:25], v[28:29], v[28:29]
	v_exp_f32_e32 v27, v27
	v_exp_f32_e32 v20, v20
	v_pk_fma_f32 v[26:27], v[26:27], v[30:31], v[30:31]
	v_exp_f32_e32 v21, v21
	v_pk_add_f32 v[28:29], v[28:29], 2.0 op_sel_hi:[1,0] neg_lo:[1,0] neg_hi:[1,0]
	v_exp_f32_e32 v22, v22
	v_pk_add_f32 v[30:31], v[30:31], 2.0 op_sel_hi:[1,0] neg_lo:[1,0] neg_hi:[1,0]
	v_exp_f32_e32 v23, v23
	v_pk_fma_f32 v[28:29], v[28:29], v[20:21], v[28:29]
	v_pk_fma_f32 v[20:21], v[20:21], v[24:25], v[24:25]
	v_pk_fma_f32 v[30:31], v[30:31], v[22:23], v[30:31]
	v_pk_fma_f32 v[22:23], v[22:23], v[26:27], v[26:27]
	v_rcp_f32_e32 v20, v20
	v_rcp_f32_e32 v21, v21
	v_rcp_f32_e32 v22, v22
	v_rcp_f32_e32 v23, v23
	v_pk_fma_f32 v[28:29], v[148:149], v[24:25], v[28:29]
	v_pk_fma_f32 v[30:31], v[150:151], v[26:27], v[30:31]
	v_pk_mul_f32 v[20:21], v[20:21], v[28:29]
	v_pk_mul_f32 v[22:23], v[22:23], v[30:31]
	v_lshl_add_u64 v[24:25], v[176:177], 0, s[16:17]
	global_store_dwordx4 v[24:25], v[20:23], off sc1
	s_nop 1
	v_pk_mul_f32 v[20:21], v[20:21], s[96:97] op_sel_hi:[1,0]
	v_pk_mul_f32 v[22:23], v[22:23], s[96:97] op_sel_hi:[1,0]
	v_exp_f32_e32 v16, v16
	v_exp_f32_e32 v17, v17
	v_exp_f32_e32 v18, v18
	v_pk_fma_f32 v[16:17], v[16:17], s[98:99], s[98:99] op_sel_hi:[1,0,0]
	v_exp_f32_e32 v19, v19
	v_exp_f32_e32 v20, v20
	v_pk_fma_f32 v[18:19], v[18:19], s[98:99], s[98:99] op_sel_hi:[1,0,0]
	v_exp_f32_e32 v21, v21
	v_exp_f32_e32 v22, v22
	v_pk_fma_f32 v[16:17], v[20:21], v[16:17], v[16:17]
	v_exp_f32_e32 v23, v23
	v_pk_add_f32 v[20:21], v[20:21], 1.0 op_sel_hi:[1,0] neg_lo:[1,0] neg_hi:[1,0]
	v_rcp_f32_e32 v16, v16
	v_rcp_f32_e32 v17, v17
	v_pk_fma_f32 v[18:19], v[22:23], v[18:19], v[18:19]
	v_pk_add_f32 v[22:23], v[22:23], 1.0 op_sel_hi:[1,0] neg_lo:[1,0] neg_hi:[1,0]
	v_rcp_f32_e32 v18, v18
	v_rcp_f32_e32 v19, v19
	v_pk_mul_f32 v[16:17], v[16:17], v[20:21]
	v_pk_mul_f32 v[18:19], v[18:19], v[22:23]
	v_cvt_pk_fp8_f32 v24, v16, v17
	v_or_b32_e32 v20, 32, v200
	v_ashrrev_i32_e32 v21, 31, v20
	v_lshlrev_b64 v[20:21], 10, v[20:21]
	v_cvt_pk_fp8_f32 v24, v18, v19 op_sel:[0,0,1]
	v_lshl_add_u64 v[22:23], v[122:123], 0, v[20:21]
	global_store_dword v[22:23], v24, off sc1
	v_exp_f32_e32 v12, v12
	v_exp_f32_e32 v13, v13
	v_exp_f32_e32 v14, v14
	v_pk_add_f32 v[12:13], v[12:13], 1.0 op_sel_hi:[1,0]
	v_exp_f32_e32 v15, v15
	v_exp_f32_e32 v8, v8
	v_pk_add_f32 v[14:15], v[14:15], 1.0 op_sel_hi:[1,0]
	v_exp_f32_e32 v9, v9
	v_exp_f32_e32 v10, v10
	v_pk_fma_f32 v[8:9], v[8:9], v[12:13], v[12:13]
	v_exp_f32_e32 v11, v11
	v_exp_f32_e32 v4, v4
	v_pk_fma_f32 v[10:11], v[10:11], v[14:15], v[14:15]
	v_exp_f32_e32 v5, v5
	v_pk_add_f32 v[12:13], v[12:13], 2.0 op_sel_hi:[1,0] neg_lo:[1,0] neg_hi:[1,0]
	v_exp_f32_e32 v6, v6
	v_pk_add_f32 v[14:15], v[14:15], 2.0 op_sel_hi:[1,0] neg_lo:[1,0] neg_hi:[1,0]
	v_exp_f32_e32 v7, v7
	v_pk_fma_f32 v[12:13], v[12:13], v[4:5], v[12:13]
	v_pk_fma_f32 v[4:5], v[4:5], v[8:9], v[8:9]
	v_pk_fma_f32 v[14:15], v[14:15], v[6:7], v[14:15]
	v_pk_fma_f32 v[6:7], v[6:7], v[10:11], v[10:11]
	v_rcp_f32_e32 v4, v4
	v_rcp_f32_e32 v5, v5
	v_rcp_f32_e32 v6, v6
	v_rcp_f32_e32 v7, v7
	v_pk_fma_f32 v[12:13], v[144:145], v[8:9], v[12:13]
	v_pk_fma_f32 v[14:15], v[146:147], v[10:11], v[14:15]
	v_lshl_add_u64 v[8:9], v[176:177], 0, s[24:25]
	v_pk_mul_f32 v[4:5], v[4:5], v[12:13]
	v_pk_mul_f32 v[6:7], v[6:7], v[14:15]
	global_store_dwordx4 v[8:9], v[4:7], off sc1
	s_nop 1
	v_pk_mul_f32 v[4:5], v[4:5], s[96:97] op_sel_hi:[1,0]
	v_pk_mul_f32 v[6:7], v[6:7], s[96:97] op_sel_hi:[1,0]
	v_exp_f32_e32 v0, v0
	v_exp_f32_e32 v1, v1
	v_exp_f32_e32 v2, v2
	v_pk_fma_f32 v[0:1], v[0:1], s[98:99], s[98:99] op_sel_hi:[1,0,0]
	v_exp_f32_e32 v3, v3
	v_exp_f32_e32 v4, v4
	v_pk_fma_f32 v[2:3], v[2:3], s[98:99], s[98:99] op_sel_hi:[1,0,0]
	v_exp_f32_e32 v5, v5
	v_exp_f32_e32 v6, v6
	v_pk_fma_f32 v[0:1], v[4:5], v[0:1], v[0:1]
	v_exp_f32_e32 v7, v7
	v_pk_add_f32 v[4:5], v[4:5], 1.0 op_sel_hi:[1,0] neg_lo:[1,0] neg_hi:[1,0]
	v_rcp_f32_e32 v0, v0
	v_rcp_f32_e32 v1, v1
	v_pk_fma_f32 v[2:3], v[6:7], v[2:3], v[2:3]
	v_pk_add_f32 v[6:7], v[6:7], 1.0 op_sel_hi:[1,0] neg_lo:[1,0] neg_hi:[1,0]
	v_rcp_f32_e32 v2, v2
	v_rcp_f32_e32 v3, v3
	v_pk_mul_f32 v[0:1], v[0:1], v[4:5]
	v_pk_mul_f32 v[2:3], v[2:3], v[6:7]
	v_cvt_pk_fp8_f32 v8, v0, v1
	v_or_b32_e32 v4, 48, v200
	v_ashrrev_i32_e32 v5, 31, v4
	v_lshlrev_b64 v[4:5], 10, v[4:5]
	v_cvt_pk_fp8_f32 v8, v2, v3 op_sel:[0,0,1]
	v_lshl_add_u64 v[6:7], v[122:123], 0, v[4:5]
	global_store_dword v[6:7], v8, off sc1
	s_branch .LBB2_24
.Lmy_epi_l7:
	v_exp_f32_e32 v124, v124
	v_exp_f32_e32 v125, v125
	v_exp_f32_e32 v126, v126
	v_pk_add_f32 v[124:125], v[124:125], 1.0 op_sel_hi:[1,0]
	v_exp_f32_e32 v127, v127
	v_exp_f32_e32 v120, v120
	v_pk_add_f32 v[126:127], v[126:127], 1.0 op_sel_hi:[1,0]
	v_exp_f32_e32 v121, v121
	v_exp_f32_e32 v122, v122
	v_pk_fma_f32 v[120:121], v[120:121], v[124:125], v[124:125]
	v_exp_f32_e32 v123, v123
	v_exp_f32_e32 v116, v116
	v_pk_fma_f32 v[122:123], v[122:123], v[126:127], v[126:127]
	v_exp_f32_e32 v117, v117
	v_pk_add_f32 v[124:125], v[124:125], 2.0 op_sel_hi:[1,0] neg_lo:[1,0] neg_hi:[1,0]
	v_exp_f32_e32 v118, v118
	v_pk_add_f32 v[126:127], v[126:127], 2.0 op_sel_hi:[1,0] neg_lo:[1,0] neg_hi:[1,0]
	v_exp_f32_e32 v119, v119
	v_pk_fma_f32 v[124:125], v[124:125], v[116:117], v[124:125]
	v_pk_fma_f32 v[116:117], v[116:117], v[120:121], v[120:121]
	v_pk_fma_f32 v[126:127], v[126:127], v[118:119], v[126:127]
	v_pk_fma_f32 v[118:119], v[118:119], v[122:123], v[122:123]
	v_rcp_f32_e32 v116, v116
	v_rcp_f32_e32 v117, v117
	v_rcp_f32_e32 v118, v118
	v_rcp_f32_e32 v119, v119
	s_waitcnt lgkmcnt(3)
	v_pk_fma_f32 v[124:125], v[172:173], v[120:121], v[124:125]
	v_pk_fma_f32 v[126:127], v[174:175], v[122:123], v[126:127]
	v_pk_mul_f32 v[116:117], v[116:117], v[124:125]
	v_pk_mul_f32 v[118:119], v[118:119], v[126:127]
	global_store_dwordx4 v[176:177], v[116:119], off sc1
	s_nop 1
	v_pk_mul_f32 v[116:117], v[116:117], s[96:97] op_sel_hi:[1,0]
	v_pk_mul_f32 v[118:119], v[118:119], s[96:97] op_sel_hi:[1,0]
	v_exp_f32_e32 v112, v112
	v_exp_f32_e32 v113, v113
	v_exp_f32_e32 v114, v114
	v_pk_fma_f32 v[112:113], v[112:113], s[98:99], s[98:99] op_sel_hi:[1,0,0]
	v_exp_f32_e32 v115, v115
	v_exp_f32_e32 v116, v116
	v_pk_fma_f32 v[114:115], v[114:115], s[98:99], s[98:99] op_sel_hi:[1,0,0]
	v_exp_f32_e32 v117, v117
	v_exp_f32_e32 v118, v118
	v_pk_fma_f32 v[112:113], v[116:117], v[112:113], v[112:113]
	v_exp_f32_e32 v119, v119
	v_pk_add_f32 v[116:117], v[116:117], 1.0 op_sel_hi:[1,0] neg_lo:[1,0] neg_hi:[1,0]
	v_rcp_f32_e32 v112, v112
	v_rcp_f32_e32 v113, v113
	v_pk_fma_f32 v[114:115], v[118:119], v[114:115], v[114:115]
	v_pk_add_f32 v[118:119], v[118:119], 1.0 op_sel_hi:[1,0] neg_lo:[1,0] neg_hi:[1,0]
	v_rcp_f32_e32 v114, v114
	v_rcp_f32_e32 v115, v115
	v_pk_mul_f32 v[112:113], v[112:113], v[116:117]
	v_pk_mul_f32 v[114:115], v[114:115], v[118:119]
	v_cvt_pk_fp8_f32 v124, v112, v113
	s_add_u32 s0, s8, s27
	s_addc_u32 s1, s9, 0
	s_ashr_i32 s35, s34, 31
	s_lshl_b64 s[34:35], s[34:35], 21
	v_ashrrev_i32_e32 v209, 31, v208
	s_add_u32 s36, s73, s34
	v_lshrrev_b32_e32 v126, 4, v210
	v_and_b32_e32 v127, 15, v210
	v_lshl_or_b32 v126, v126, 8, v127
	v_and_b32_e32 v127, 15, v208
	v_mul_u32_u24_e32 v127, 0x3f0, v127
	v_sub_u32_e32 v126, v126, v127
	v_ashrrev_i32_e32 v127, 31, v126
	v_lshl_add_u64 v[122:123], s[0:1], 0, v[126:127]
	v_cvt_pk_fp8_f32 v124, v114, v115 op_sel:[0,0,1]
	v_lshlrev_b64 v[116:117], 10, v[208:209]
	s_addc_u32 s37, s74, s35
	v_lshl_add_u64 v[118:119], v[122:123], 0, v[116:117]
	global_store_dword v[118:119], v124, off sc1
	s_cmp_eq_u32 s30, 7
	s_cselect_b64 s[34:35], -1, 0
	s_cmp_lg_u32 s30, 7
	v_lshrrev_b32_e32 v126, 4, v210
	v_lshlrev_b32_e32 v126, 9, v126
	v_and_b32_e32 v127, 15, v210
	v_lshl_or_b32 v126, v127, 1, v126
	v_and_b32_e32 v127, 15, v208
	v_mul_u32_u24_e32 v127, 0x7e0, v127
	v_sub_u32_e32 v126, v126, v127
	v_ashrrev_i32_e32 v127, 31, v126
	v_lshl_add_u64 v[120:121], s[36:37], 0, v[126:127]
	v_pk_mul_f32 v[112:113], v[112:113], s[98:99] op_sel_hi:[1,0]
	v_pk_mul_f32 v[114:115], v[114:115], s[98:99] op_sel_hi:[1,0]
	v_cvt_pk_f16_f32 v112, v112, v113
	v_cvt_pk_f16_f32 v113, v114, v115
	v_lshl_add_u64 v[114:115], v[116:117], 1, v[120:121]
	global_store_dwordx2 v[114:115], v[112:113], off sc1
	v_exp_f32_e32 v108, v108
	v_exp_f32_e32 v109, v109
	v_exp_f32_e32 v110, v110
	v_pk_add_f32 v[108:109], v[108:109], 1.0 op_sel_hi:[1,0]
	v_exp_f32_e32 v111, v111
	v_exp_f32_e32 v104, v104
	v_pk_add_f32 v[110:111], v[110:111], 1.0 op_sel_hi:[1,0]
	v_exp_f32_e32 v105, v105
	v_exp_f32_e32 v106, v106
	v_pk_fma_f32 v[104:105], v[104:105], v[108:109], v[108:109]
	v_exp_f32_e32 v107, v107
	v_exp_f32_e32 v100, v100
	v_pk_fma_f32 v[106:107], v[106:107], v[110:111], v[110:111]
	v_exp_f32_e32 v101, v101
	v_pk_add_f32 v[108:109], v[108:109], 2.0 op_sel_hi:[1,0] neg_lo:[1,0] neg_hi:[1,0]
	v_exp_f32_e32 v102, v102
	v_pk_add_f32 v[110:111], v[110:111], 2.0 op_sel_hi:[1,0] neg_lo:[1,0] neg_hi:[1,0]
	v_exp_f32_e32 v103, v103
	v_pk_fma_f32 v[108:109], v[108:109], v[100:101], v[108:109]
	v_pk_fma_f32 v[100:101], v[100:101], v[104:105], v[104:105]
	v_pk_fma_f32 v[110:111], v[110:111], v[102:103], v[110:111]
	v_pk_fma_f32 v[102:103], v[102:103], v[106:107], v[106:107]
	v_rcp_f32_e32 v100, v100
	v_rcp_f32_e32 v101, v101
	v_rcp_f32_e32 v102, v102
	v_rcp_f32_e32 v103, v103
	s_waitcnt lgkmcnt(2)
	v_pk_fma_f32 v[108:109], v[168:169], v[104:105], v[108:109]
	v_pk_fma_f32 v[110:111], v[170:171], v[106:107], v[110:111]
	v_lshl_add_u64 v[104:105], v[176:177], 0, s[18:19]
	v_pk_mul_f32 v[100:101], v[100:101], v[108:109]
	v_pk_mul_f32 v[102:103], v[102:103], v[110:111]
	global_store_dwordx4 v[104:105], v[100:103], off sc1
	s_nop 1
	v_pk_mul_f32 v[100:101], v[100:101], s[96:97] op_sel_hi:[1,0]
	v_pk_mul_f32 v[102:103], v[102:103], s[96:97] op_sel_hi:[1,0]
	v_exp_f32_e32 v96, v96
	v_exp_f32_e32 v97, v97
	v_exp_f32_e32 v98, v98
	v_pk_fma_f32 v[96:97], v[96:97], s[98:99], s[98:99] op_sel_hi:[1,0,0]
	v_exp_f32_e32 v99, v99
	v_exp_f32_e32 v100, v100
	v_pk_fma_f32 v[98:99], v[98:99], s[98:99], s[98:99] op_sel_hi:[1,0,0]
	v_exp_f32_e32 v101, v101
	v_exp_f32_e32 v102, v102
	v_pk_fma_f32 v[96:97], v[100:101], v[96:97], v[96:97]
	v_exp_f32_e32 v103, v103
	v_pk_add_f32 v[100:101], v[100:101], 1.0 op_sel_hi:[1,0] neg_lo:[1,0] neg_hi:[1,0]
	v_rcp_f32_e32 v96, v96
	v_rcp_f32_e32 v97, v97
	v_pk_fma_f32 v[98:99], v[102:103], v[98:99], v[98:99]
	v_pk_add_f32 v[102:103], v[102:103], 1.0 op_sel_hi:[1,0] neg_lo:[1,0] neg_hi:[1,0]
	v_rcp_f32_e32 v98, v98
	v_rcp_f32_e32 v99, v99
	v_pk_mul_f32 v[96:97], v[96:97], v[100:101]
	v_pk_mul_f32 v[98:99], v[98:99], v[102:103]
	v_cvt_pk_fp8_f32 v104, v96, v97
	v_ashrrev_i32_e32 v207, 31, v206
	v_lshlrev_b64 v[100:101], 10, v[206:207]
	v_lshl_add_u64 v[102:103], v[122:123], 0, v[100:101]
	v_cvt_pk_fp8_f32 v104, v98, v99 op_sel:[0,0,1]
	v_cndmask_b32_e64 v105, 0, 1, s[34:35]
	global_store_dword v[102:103], v104, off sc1
	v_cmp_ne_u32_e64 s[0:1], 1, v105
	v_pk_mul_f32 v[96:97], v[96:97], s[98:99] op_sel_hi:[1,0]
	v_pk_mul_f32 v[98:99], v[98:99], s[98:99] op_sel_hi:[1,0]
	v_cvt_pk_f16_f32 v96, v96, v97
	v_cvt_pk_f16_f32 v97, v98, v99
	v_lshl_add_u64 v[98:99], v[100:101], 1, v[120:121]
	global_store_dwordx2 v[98:99], v[96:97], off sc1
	v_exp_f32_e32 v92, v92
	v_exp_f32_e32 v93, v93
	v_exp_f32_e32 v94, v94
	v_pk_add_f32 v[92:93], v[92:93], 1.0 op_sel_hi:[1,0]
	v_exp_f32_e32 v95, v95
	v_exp_f32_e32 v88, v88
	v_pk_add_f32 v[94:95], v[94:95], 1.0 op_sel_hi:[1,0]
	v_exp_f32_e32 v89, v89
	v_exp_f32_e32 v90, v90
	v_pk_fma_f32 v[88:89], v[88:89], v[92:93], v[92:93]
	v_exp_f32_e32 v91, v91
	v_exp_f32_e32 v84, v84
	v_pk_fma_f32 v[90:91], v[90:91], v[94:95], v[94:95]
	v_exp_f32_e32 v85, v85
	v_pk_add_f32 v[92:93], v[92:93], 2.0 op_sel_hi:[1,0] neg_lo:[1,0] neg_hi:[1,0]
	v_exp_f32_e32 v86, v86
	v_pk_add_f32 v[94:95], v[94:95], 2.0 op_sel_hi:[1,0] neg_lo:[1,0] neg_hi:[1,0]
	v_exp_f32_e32 v87, v87
	v_pk_fma_f32 v[92:93], v[92:93], v[84:85], v[92:93]
	v_pk_fma_f32 v[84:85], v[84:85], v[88:89], v[88:89]
	v_pk_fma_f32 v[94:95], v[94:95], v[86:87], v[94:95]
	v_pk_fma_f32 v[86:87], v[86:87], v[90:91], v[90:91]
	v_rcp_f32_e32 v84, v84
	v_rcp_f32_e32 v85, v85
	v_rcp_f32_e32 v86, v86
	v_rcp_f32_e32 v87, v87
	s_waitcnt lgkmcnt(1)
	v_pk_fma_f32 v[92:93], v[164:165], v[88:89], v[92:93]
	v_pk_fma_f32 v[94:95], v[166:167], v[90:91], v[94:95]
	v_pk_mul_f32 v[84:85], v[84:85], v[92:93]
	v_pk_mul_f32 v[86:87], v[86:87], v[94:95]
	v_lshl_add_u64 v[88:89], v[176:177], 0, s[12:13]
	global_store_dwordx4 v[88:89], v[84:87], off sc1
	s_nop 1
	v_pk_mul_f32 v[84:85], v[84:85], s[96:97] op_sel_hi:[1,0]
	v_pk_mul_f32 v[86:87], v[86:87], s[96:97] op_sel_hi:[1,0]
	v_exp_f32_e32 v80, v80
	v_exp_f32_e32 v81, v81
	v_exp_f32_e32 v82, v82
	v_pk_fma_f32 v[80:81], v[80:81], s[98:99], s[98:99] op_sel_hi:[1,0,0]
	v_exp_f32_e32 v83, v83
	v_exp_f32_e32 v84, v84
	v_pk_fma_f32 v[82:83], v[82:83], s[98:99], s[98:99] op_sel_hi:[1,0,0]
	v_exp_f32_e32 v85, v85
	v_exp_f32_e32 v86, v86
	v_pk_fma_f32 v[80:81], v[84:85], v[80:81], v[80:81]
	v_exp_f32_e32 v87, v87
	v_pk_add_f32 v[84:85], v[84:85], 1.0 op_sel_hi:[1,0] neg_lo:[1,0] neg_hi:[1,0]
	v_rcp_f32_e32 v80, v80
	v_rcp_f32_e32 v81, v81
	v_pk_fma_f32 v[82:83], v[86:87], v[82:83], v[82:83]
	v_pk_add_f32 v[86:87], v[86:87], 1.0 op_sel_hi:[1,0] neg_lo:[1,0] neg_hi:[1,0]
	v_rcp_f32_e32 v82, v82
	v_rcp_f32_e32 v83, v83
	v_pk_mul_f32 v[80:81], v[80:81], v[84:85]
	v_pk_mul_f32 v[82:83], v[82:83], v[86:87]
	v_ashrrev_i32_e32 v205, 31, v204
	v_cvt_pk_fp8_f32 v88, v80, v81
	s_and_b64 vcc, exec, s[0:1]
	v_cvt_pk_fp8_f32 v88, v82, v83 op_sel:[0,0,1]
	v_lshlrev_b64 v[84:85], 10, v[204:205]
	v_lshl_add_u64 v[86:87], v[122:123], 0, v[84:85]
	global_store_dword v[86:87], v88, off sc1
	v_pk_mul_f32 v[80:81], v[80:81], s[98:99] op_sel_hi:[1,0]
	v_pk_mul_f32 v[82:83], v[82:83], s[98:99] op_sel_hi:[1,0]
	v_cvt_pk_f16_f32 v80, v80, v81
	v_cvt_pk_f16_f32 v81, v82, v83
	v_lshl_add_u64 v[82:83], v[84:85], 1, v[120:121]
	global_store_dwordx2 v[82:83], v[80:81], off sc1
	v_exp_f32_e32 v76, v76
	v_exp_f32_e32 v77, v77
	v_exp_f32_e32 v78, v78
	v_pk_add_f32 v[76:77], v[76:77], 1.0 op_sel_hi:[1,0]
	v_exp_f32_e32 v79, v79
	v_exp_f32_e32 v72, v72
	v_pk_add_f32 v[78:79], v[78:79], 1.0 op_sel_hi:[1,0]
	v_exp_f32_e32 v73, v73
	v_exp_f32_e32 v74, v74
	v_pk_fma_f32 v[72:73], v[72:73], v[76:77], v[76:77]
	v_exp_f32_e32 v75, v75
	v_exp_f32_e32 v68, v68
	v_pk_fma_f32 v[74:75], v[74:75], v[78:79], v[78:79]
	v_exp_f32_e32 v69, v69
	v_pk_add_f32 v[76:77], v[76:77], 2.0 op_sel_hi:[1,0] neg_lo:[1,0] neg_hi:[1,0]
	v_exp_f32_e32 v70, v70
	v_pk_add_f32 v[78:79], v[78:79], 2.0 op_sel_hi:[1,0] neg_lo:[1,0] neg_hi:[1,0]
	v_exp_f32_e32 v71, v71
	v_pk_fma_f32 v[76:77], v[76:77], v[68:69], v[76:77]
	v_pk_fma_f32 v[68:69], v[68:69], v[72:73], v[72:73]
	v_pk_fma_f32 v[78:79], v[78:79], v[70:71], v[78:79]
	v_pk_fma_f32 v[70:71], v[70:71], v[74:75], v[74:75]
	v_rcp_f32_e32 v68, v68
	v_rcp_f32_e32 v69, v69
	v_rcp_f32_e32 v70, v70
	v_rcp_f32_e32 v71, v71
	s_waitcnt lgkmcnt(0)
	v_pk_fma_f32 v[76:77], v[160:161], v[72:73], v[76:77]
	v_pk_fma_f32 v[78:79], v[162:163], v[74:75], v[78:79]
	v_lshl_add_u64 v[72:73], v[176:177], 0, s[20:21]
	v_pk_mul_f32 v[68:69], v[68:69], v[76:77]
	v_pk_mul_f32 v[70:71], v[70:71], v[78:79]
	global_store_dwordx4 v[72:73], v[68:71], off sc1
	s_nop 1
	v_pk_mul_f32 v[68:69], v[68:69], s[96:97] op_sel_hi:[1,0]
	v_pk_mul_f32 v[70:71], v[70:71], s[96:97] op_sel_hi:[1,0]
	v_exp_f32_e32 v64, v64
	v_exp_f32_e32 v65, v65
	v_exp_f32_e32 v66, v66
	v_pk_fma_f32 v[64:65], v[64:65], s[98:99], s[98:99] op_sel_hi:[1,0,0]
	v_exp_f32_e32 v67, v67
	v_exp_f32_e32 v68, v68
	v_pk_fma_f32 v[66:67], v[66:67], s[98:99], s[98:99] op_sel_hi:[1,0,0]
	v_exp_f32_e32 v69, v69
	v_exp_f32_e32 v70, v70
	v_pk_fma_f32 v[64:65], v[68:69], v[64:65], v[64:65]
	v_exp_f32_e32 v71, v71
	v_pk_add_f32 v[68:69], v[68:69], 1.0 op_sel_hi:[1,0] neg_lo:[1,0] neg_hi:[1,0]
	v_rcp_f32_e32 v64, v64
	v_rcp_f32_e32 v65, v65
	v_pk_fma_f32 v[66:67], v[70:71], v[66:67], v[66:67]
	v_pk_add_f32 v[70:71], v[70:71], 1.0 op_sel_hi:[1,0] neg_lo:[1,0] neg_hi:[1,0]
	v_rcp_f32_e32 v66, v66
	v_rcp_f32_e32 v67, v67
	v_pk_mul_f32 v[64:65], v[64:65], v[68:69]
	v_pk_mul_f32 v[66:67], v[66:67], v[70:71]
	v_ashrrev_i32_e32 v203, 31, v202
	v_cvt_pk_fp8_f32 v72, v64, v65
	s_and_b64 vcc, exec, s[0:1]
	v_cvt_pk_fp8_f32 v72, v66, v67 op_sel:[0,0,1]
	v_lshlrev_b64 v[68:69], 10, v[202:203]
	v_lshl_add_u64 v[70:71], v[122:123], 0, v[68:69]
	global_store_dword v[70:71], v72, off sc1
	v_pk_mul_f32 v[64:65], v[64:65], s[98:99] op_sel_hi:[1,0]
	v_pk_mul_f32 v[66:67], v[66:67], s[98:99] op_sel_hi:[1,0]
	v_cvt_pk_f16_f32 v64, v64, v65
	v_cvt_pk_f16_f32 v65, v66, v67
	v_lshl_add_u64 v[66:67], v[68:69], 1, v[120:121]
	global_store_dwordx2 v[66:67], v[64:65], off sc1
	v_exp_f32_e32 v60, v60
	v_exp_f32_e32 v61, v61
	v_exp_f32_e32 v62, v62
	v_pk_add_f32 v[60:61], v[60:61], 1.0 op_sel_hi:[1,0]
	v_exp_f32_e32 v63, v63
	v_exp_f32_e32 v56, v56
	v_pk_add_f32 v[62:63], v[62:63], 1.0 op_sel_hi:[1,0]
	v_exp_f32_e32 v57, v57
	v_exp_f32_e32 v58, v58
	v_pk_fma_f32 v[56:57], v[56:57], v[60:61], v[60:61]
	v_exp_f32_e32 v59, v59
	v_exp_f32_e32 v52, v52
	v_pk_fma_f32 v[58:59], v[58:59], v[62:63], v[62:63]
	v_exp_f32_e32 v53, v53
	v_pk_add_f32 v[60:61], v[60:61], 2.0 op_sel_hi:[1,0] neg_lo:[1,0] neg_hi:[1,0]
	v_exp_f32_e32 v54, v54
	v_pk_add_f32 v[62:63], v[62:63], 2.0 op_sel_hi:[1,0] neg_lo:[1,0] neg_hi:[1,0]
	v_exp_f32_e32 v55, v55
	v_pk_fma_f32 v[60:61], v[60:61], v[52:53], v[60:61]
	v_pk_fma_f32 v[52:53], v[52:53], v[56:57], v[56:57]
	v_pk_fma_f32 v[62:63], v[62:63], v[54:55], v[62:63]
	v_pk_fma_f32 v[54:55], v[54:55], v[58:59], v[58:59]
	v_rcp_f32_e32 v52, v52
	v_rcp_f32_e32 v53, v53
	v_rcp_f32_e32 v54, v54
	v_rcp_f32_e32 v55, v55
	s_waitcnt vmcnt(8)
	v_pk_fma_f32 v[60:61], v[156:157], v[56:57], v[60:61]
	v_pk_fma_f32 v[62:63], v[158:159], v[58:59], v[62:63]
	v_pk_mul_f32 v[52:53], v[52:53], v[60:61]
	v_pk_mul_f32 v[54:55], v[54:55], v[62:63]
	v_lshl_add_u64 v[56:57], v[176:177], 0, s[14:15]
	global_store_dwordx4 v[56:57], v[52:55], off sc1
	s_nop 1
	v_pk_mul_f32 v[52:53], v[52:53], s[96:97] op_sel_hi:[1,0]
	v_pk_mul_f32 v[54:55], v[54:55], s[96:97] op_sel_hi:[1,0]
	v_exp_f32_e32 v48, v48
	v_exp_f32_e32 v49, v49
	v_exp_f32_e32 v50, v50
	v_pk_fma_f32 v[48:49], v[48:49], s[98:99], s[98:99] op_sel_hi:[1,0,0]
	v_exp_f32_e32 v51, v51
	v_exp_f32_e32 v52, v52
	v_pk_fma_f32 v[50:51], v[50:51], s[98:99], s[98:99] op_sel_hi:[1,0,0]
	v_exp_f32_e32 v53, v53
	v_exp_f32_e32 v54, v54
	v_pk_fma_f32 v[48:49], v[52:53], v[48:49], v[48:49]
	v_exp_f32_e32 v55, v55
	v_pk_add_f32 v[52:53], v[52:53], 1.0 op_sel_hi:[1,0] neg_lo:[1,0] neg_hi:[1,0]
	v_rcp_f32_e32 v48, v48
	v_rcp_f32_e32 v49, v49
	v_pk_fma_f32 v[50:51], v[54:55], v[50:51], v[50:51]
	v_pk_add_f32 v[54:55], v[54:55], 1.0 op_sel_hi:[1,0] neg_lo:[1,0] neg_hi:[1,0]
	v_rcp_f32_e32 v50, v50
	v_rcp_f32_e32 v51, v51
	v_pk_mul_f32 v[48:49], v[48:49], v[52:53]
	v_pk_mul_f32 v[50:51], v[50:51], v[54:55]
	v_ashrrev_i32_e32 v201, 31, v200
	v_cvt_pk_fp8_f32 v56, v48, v49
	s_and_b64 vcc, exec, s[0:1]
	v_cvt_pk_fp8_f32 v56, v50, v51 op_sel:[0,0,1]
	v_lshlrev_b64 v[52:53], 10, v[200:201]
	v_lshl_add_u64 v[54:55], v[122:123], 0, v[52:53]
	global_store_dword v[54:55], v56, off sc1
	v_pk_mul_f32 v[48:49], v[48:49], s[98:99] op_sel_hi:[1,0]
	v_pk_mul_f32 v[50:51], v[50:51], s[98:99] op_sel_hi:[1,0]
	v_cvt_pk_f16_f32 v48, v48, v49
	v_cvt_pk_f16_f32 v49, v50, v51
	v_lshl_add_u64 v[50:51], v[52:53], 1, v[120:121]
	global_store_dwordx2 v[50:51], v[48:49], off sc1
	v_exp_f32_e32 v44, v44
	v_exp_f32_e32 v45, v45
	v_exp_f32_e32 v46, v46
	v_pk_add_f32 v[44:45], v[44:45], 1.0 op_sel_hi:[1,0]
	v_exp_f32_e32 v47, v47
	v_exp_f32_e32 v40, v40
	v_pk_add_f32 v[46:47], v[46:47], 1.0 op_sel_hi:[1,0]
	v_exp_f32_e32 v41, v41
	v_exp_f32_e32 v42, v42
	v_pk_fma_f32 v[40:41], v[40:41], v[44:45], v[44:45]
	v_exp_f32_e32 v43, v43
	v_exp_f32_e32 v36, v36
	v_pk_fma_f32 v[42:43], v[42:43], v[46:47], v[46:47]
	v_exp_f32_e32 v37, v37
	v_pk_add_f32 v[44:45], v[44:45], 2.0 op_sel_hi:[1,0] neg_lo:[1,0] neg_hi:[1,0]
	v_exp_f32_e32 v38, v38
	v_pk_add_f32 v[46:47], v[46:47], 2.0 op_sel_hi:[1,0] neg_lo:[1,0] neg_hi:[1,0]
	v_exp_f32_e32 v39, v39
	v_pk_fma_f32 v[44:45], v[44:45], v[36:37], v[44:45]
	v_pk_fma_f32 v[36:37], v[36:37], v[40:41], v[40:41]
	v_pk_fma_f32 v[46:47], v[46:47], v[38:39], v[46:47]
	v_pk_fma_f32 v[38:39], v[38:39], v[42:43], v[42:43]
	v_rcp_f32_e32 v36, v36
	v_rcp_f32_e32 v37, v37
	v_rcp_f32_e32 v38, v38
	v_rcp_f32_e32 v39, v39
	v_pk_fma_f32 v[44:45], v[152:153], v[40:41], v[44:45]
	v_pk_fma_f32 v[46:47], v[154:155], v[42:43], v[46:47]
	v_lshl_add_u64 v[40:41], v[176:177], 0, s[22:23]
	v_pk_mul_f32 v[36:37], v[36:37], v[44:45]
	v_pk_mul_f32 v[38:39], v[38:39], v[46:47]
	global_store_dwordx4 v[40:41], v[36:39], off sc1
	s_nop 1
	v_pk_mul_f32 v[36:37], v[36:37], s[96:97] op_sel_hi:[1,0]
	v_pk_mul_f32 v[38:39], v[38:39], s[96:97] op_sel_hi:[1,0]
	v_exp_f32_e32 v32, v32
	v_exp_f32_e32 v33, v33
	v_exp_f32_e32 v34, v34
	v_pk_fma_f32 v[32:33], v[32:33], s[98:99], s[98:99] op_sel_hi:[1,0,0]
	v_exp_f32_e32 v35, v35
	v_exp_f32_e32 v36, v36
	v_pk_fma_f32 v[34:35], v[34:35], s[98:99], s[98:99] op_sel_hi:[1,0,0]
	v_exp_f32_e32 v37, v37
	v_exp_f32_e32 v38, v38
	v_pk_fma_f32 v[32:33], v[36:37], v[32:33], v[32:33]
	v_exp_f32_e32 v39, v39
	v_pk_add_f32 v[36:37], v[36:37], 1.0 op_sel_hi:[1,0] neg_lo:[1,0] neg_hi:[1,0]
	v_rcp_f32_e32 v32, v32
	v_rcp_f32_e32 v33, v33
	v_pk_fma_f32 v[34:35], v[38:39], v[34:35], v[34:35]
	v_pk_add_f32 v[38:39], v[38:39], 1.0 op_sel_hi:[1,0] neg_lo:[1,0] neg_hi:[1,0]
	v_rcp_f32_e32 v34, v34
	v_rcp_f32_e32 v35, v35
	v_pk_mul_f32 v[32:33], v[32:33], v[36:37]
	v_pk_mul_f32 v[34:35], v[34:35], v[38:39]
	v_cvt_pk_fp8_f32 v40, v32, v33
	v_or_b32_e32 v36, 16, v200
	v_ashrrev_i32_e32 v37, 31, v36
	v_lshlrev_b64 v[36:37], 10, v[36:37]
	v_cvt_pk_fp8_f32 v40, v34, v35 op_sel:[0,0,1]
	v_lshl_add_u64 v[38:39], v[122:123], 0, v[36:37]
	global_store_dword v[38:39], v40, off sc1
	v_pk_mul_f32 v[32:33], v[32:33], s[98:99] op_sel_hi:[1,0]
	v_pk_mul_f32 v[34:35], v[34:35], s[98:99] op_sel_hi:[1,0]
	v_cvt_pk_f16_f32 v32, v32, v33
	v_cvt_pk_f16_f32 v33, v34, v35
	v_lshl_add_u64 v[34:35], v[36:37], 1, v[120:121]
	global_store_dwordx2 v[34:35], v[32:33], off sc1
	v_exp_f32_e32 v28, v28
	v_exp_f32_e32 v29, v29
	v_exp_f32_e32 v30, v30
	v_pk_add_f32 v[28:29], v[28:29], 1.0 op_sel_hi:[1,0]
	v_exp_f32_e32 v31, v31
	v_exp_f32_e32 v24, v24
	v_pk_add_f32 v[30:31], v[30:31], 1.0 op_sel_hi:[1,0]
	v_exp_f32_e32 v25, v25
	v_exp_f32_e32 v26, v26
	v_pk_fma_f32 v[24:25], v[24:25], v[28:29], v[28:29]
	v_exp_f32_e32 v27, v27
	v_exp_f32_e32 v20, v20
	v_pk_fma_f32 v[26:27], v[26:27], v[30:31], v[30:31]
	v_exp_f32_e32 v21, v21
	v_pk_add_f32 v[28:29], v[28:29], 2.0 op_sel_hi:[1,0] neg_lo:[1,0] neg_hi:[1,0]
	v_exp_f32_e32 v22, v22
	v_pk_add_f32 v[30:31], v[30:31], 2.0 op_sel_hi:[1,0] neg_lo:[1,0] neg_hi:[1,0]
	v_exp_f32_e32 v23, v23
	v_pk_fma_f32 v[28:29], v[28:29], v[20:21], v[28:29]
	v_pk_fma_f32 v[20:21], v[20:21], v[24:25], v[24:25]
	v_pk_fma_f32 v[30:31], v[30:31], v[22:23], v[30:31]
	v_pk_fma_f32 v[22:23], v[22:23], v[26:27], v[26:27]
	v_rcp_f32_e32 v20, v20
	v_rcp_f32_e32 v21, v21
	v_rcp_f32_e32 v22, v22
	v_rcp_f32_e32 v23, v23
	v_pk_fma_f32 v[28:29], v[148:149], v[24:25], v[28:29]
	v_pk_fma_f32 v[30:31], v[150:151], v[26:27], v[30:31]
	v_pk_mul_f32 v[20:21], v[20:21], v[28:29]
	v_pk_mul_f32 v[22:23], v[22:23], v[30:31]
	v_lshl_add_u64 v[24:25], v[176:177], 0, s[16:17]
	global_store_dwordx4 v[24:25], v[20:23], off sc1
	s_nop 1
	v_pk_mul_f32 v[20:21], v[20:21], s[96:97] op_sel_hi:[1,0]
	v_pk_mul_f32 v[22:23], v[22:23], s[96:97] op_sel_hi:[1,0]
	v_exp_f32_e32 v16, v16
	v_exp_f32_e32 v17, v17
	v_exp_f32_e32 v18, v18
	v_pk_fma_f32 v[16:17], v[16:17], s[98:99], s[98:99] op_sel_hi:[1,0,0]
	v_exp_f32_e32 v19, v19
	v_exp_f32_e32 v20, v20
	v_pk_fma_f32 v[18:19], v[18:19], s[98:99], s[98:99] op_sel_hi:[1,0,0]
	v_exp_f32_e32 v21, v21
	v_exp_f32_e32 v22, v22
	v_pk_fma_f32 v[16:17], v[20:21], v[16:17], v[16:17]
	v_exp_f32_e32 v23, v23
	v_pk_add_f32 v[20:21], v[20:21], 1.0 op_sel_hi:[1,0] neg_lo:[1,0] neg_hi:[1,0]
	v_rcp_f32_e32 v16, v16
	v_rcp_f32_e32 v17, v17
	v_pk_fma_f32 v[18:19], v[22:23], v[18:19], v[18:19]
	v_pk_add_f32 v[22:23], v[22:23], 1.0 op_sel_hi:[1,0] neg_lo:[1,0] neg_hi:[1,0]
	v_rcp_f32_e32 v18, v18
	v_rcp_f32_e32 v19, v19
	v_pk_mul_f32 v[16:17], v[16:17], v[20:21]
	v_pk_mul_f32 v[18:19], v[18:19], v[22:23]
	v_cvt_pk_fp8_f32 v24, v16, v17
	v_or_b32_e32 v20, 32, v200
	v_ashrrev_i32_e32 v21, 31, v20
	v_lshlrev_b64 v[20:21], 10, v[20:21]
	v_cvt_pk_fp8_f32 v24, v18, v19 op_sel:[0,0,1]
	v_lshl_add_u64 v[22:23], v[122:123], 0, v[20:21]
	global_store_dword v[22:23], v24, off sc1
	v_pk_mul_f32 v[16:17], v[16:17], s[98:99] op_sel_hi:[1,0]
	v_pk_mul_f32 v[18:19], v[18:19], s[98:99] op_sel_hi:[1,0]
	v_cvt_pk_f16_f32 v16, v16, v17
	v_cvt_pk_f16_f32 v17, v18, v19
	v_lshl_add_u64 v[18:19], v[20:21], 1, v[120:121]
	global_store_dwordx2 v[18:19], v[16:17], off sc1
	v_exp_f32_e32 v12, v12
	v_exp_f32_e32 v13, v13
	v_exp_f32_e32 v14, v14
	v_pk_add_f32 v[12:13], v[12:13], 1.0 op_sel_hi:[1,0]
	v_exp_f32_e32 v15, v15
	v_exp_f32_e32 v8, v8
	v_pk_add_f32 v[14:15], v[14:15], 1.0 op_sel_hi:[1,0]
	v_exp_f32_e32 v9, v9
	v_exp_f32_e32 v10, v10
	v_pk_fma_f32 v[8:9], v[8:9], v[12:13], v[12:13]
	v_exp_f32_e32 v11, v11
	v_exp_f32_e32 v4, v4
	v_pk_fma_f32 v[10:11], v[10:11], v[14:15], v[14:15]
	v_exp_f32_e32 v5, v5
	v_pk_add_f32 v[12:13], v[12:13], 2.0 op_sel_hi:[1,0] neg_lo:[1,0] neg_hi:[1,0]
	v_exp_f32_e32 v6, v6
	v_pk_add_f32 v[14:15], v[14:15], 2.0 op_sel_hi:[1,0] neg_lo:[1,0] neg_hi:[1,0]
	v_exp_f32_e32 v7, v7
	v_pk_fma_f32 v[12:13], v[12:13], v[4:5], v[12:13]
	v_pk_fma_f32 v[4:5], v[4:5], v[8:9], v[8:9]
	v_pk_fma_f32 v[14:15], v[14:15], v[6:7], v[14:15]
	v_pk_fma_f32 v[6:7], v[6:7], v[10:11], v[10:11]
	v_rcp_f32_e32 v4, v4
	v_rcp_f32_e32 v5, v5
	v_rcp_f32_e32 v6, v6
	v_rcp_f32_e32 v7, v7
	v_pk_fma_f32 v[12:13], v[144:145], v[8:9], v[12:13]
	v_pk_fma_f32 v[14:15], v[146:147], v[10:11], v[14:15]
	v_lshl_add_u64 v[8:9], v[176:177], 0, s[24:25]
	v_pk_mul_f32 v[4:5], v[4:5], v[12:13]
	v_pk_mul_f32 v[6:7], v[6:7], v[14:15]
	global_store_dwordx4 v[8:9], v[4:7], off sc1
	s_nop 1
	v_pk_mul_f32 v[4:5], v[4:5], s[96:97] op_sel_hi:[1,0]
	v_pk_mul_f32 v[6:7], v[6:7], s[96:97] op_sel_hi:[1,0]
	v_exp_f32_e32 v0, v0
	v_exp_f32_e32 v1, v1
	v_exp_f32_e32 v2, v2
	v_pk_fma_f32 v[0:1], v[0:1], s[98:99], s[98:99] op_sel_hi:[1,0,0]
	v_exp_f32_e32 v3, v3
	v_exp_f32_e32 v4, v4
	v_pk_fma_f32 v[2:3], v[2:3], s[98:99], s[98:99] op_sel_hi:[1,0,0]
	v_exp_f32_e32 v5, v5
	v_exp_f32_e32 v6, v6
	v_pk_fma_f32 v[0:1], v[4:5], v[0:1], v[0:1]
	v_exp_f32_e32 v7, v7
	v_pk_add_f32 v[4:5], v[4:5], 1.0 op_sel_hi:[1,0] neg_lo:[1,0] neg_hi:[1,0]
	v_rcp_f32_e32 v0, v0
	v_rcp_f32_e32 v1, v1
	v_pk_fma_f32 v[2:3], v[6:7], v[2:3], v[2:3]
	v_pk_add_f32 v[6:7], v[6:7], 1.0 op_sel_hi:[1,0] neg_lo:[1,0] neg_hi:[1,0]
	v_rcp_f32_e32 v2, v2
	v_rcp_f32_e32 v3, v3
	v_pk_mul_f32 v[0:1], v[0:1], v[4:5]
	v_pk_mul_f32 v[2:3], v[2:3], v[6:7]
	v_cvt_pk_fp8_f32 v8, v0, v1
	v_or_b32_e32 v4, 48, v200
	v_ashrrev_i32_e32 v5, 31, v4
	v_lshlrev_b64 v[4:5], 10, v[4:5]
	v_cvt_pk_fp8_f32 v8, v2, v3 op_sel:[0,0,1]
	v_lshl_add_u64 v[6:7], v[122:123], 0, v[4:5]
	global_store_dword v[6:7], v8, off sc1
	v_pk_mul_f32 v[0:1], v[0:1], s[98:99] op_sel_hi:[1,0]
	v_pk_mul_f32 v[2:3], v[2:3], s[98:99] op_sel_hi:[1,0]
	v_cvt_pk_f16_f32 v0, v0, v1
	v_cvt_pk_f16_f32 v1, v2, v3
	v_lshl_add_u64 v[2:3], v[4:5], 1, v[120:121]
	global_store_dwordx2 v[2:3], v[0:1], off sc1
	s_branch .LBB2_24
